# adds: K-loops raise priority before the pre-MFMA barrier and drop it after the post-MFMA barrier (one issue slot off each hand-off)
# speedup vs baseline: 1.0065x; 1.0016x over previous
; #define PG8_GREAD(dst, u, par) do { _Pragma("unroll") for (int h_ = 0; h_ < 2; ++h_) _Pragma("unroll") for (int i_ = 0; i_ < 2; ++i_) { const int rl_ = 128 * h_ + grl[i_]; \
;         const int tk_ = *(const PG8_LAS int*)(gtab + (par) * 2048 + rl_ * 8); const unsigned tok_ = (rl_ < (u).rows) ? ((unsigned)tk_ >> 2) : 0u; dst[h_][i_] = tok_ * (unsigned)(K * 2) + gcb[i_]; } } while (0)
; #define PG8_STAGE(bufoff, gbase, voff) do { _Pragma("unroll") for (int _i = 0; _i < 2; ++_i) \
;         __builtin_amdgcn_global_load_lds((const unsigned*)((const char*)(gbase) + (voff)[_i]), (PG8_LAS unsigned*)(lds + (bufoff) + ldsw + _i * 8192), 16, 0, 0); } while (0)
; #define PG8_WAIT_V(n) asm volatile("s_waitcnt vmcnt(" #n ")" ::: "memory")
; template <class Epi, class Sched, bool ALIGN_EPI = false, bool SP2 = false, bool GATHER = false>
; __device__ __forceinline__ void gemm_phase(PG8_LAS unsigned char* lds, const Gemm g, const Sched& S, const Epi& E, const int2* gslot = nullptr, PG8_LAS unsigned char* gtab = nullptr) {
;     ...
;             const char* a1 = cA + (size_t)(t + 1) * kstep;
;             const char* a2 = last ? nA : cA + (size_t)(t + 2) * kstep; const char* b2 = last ? nB : cB + (size_t)(t + 2) * kstep;
;             const char* a3 = a2 + kstep; const char* b3 = b2 + kstep;
;             if (last && has_next) S.a_ready(nxt);
;             if constexpr (GATHER) { if (last) { if (has_next) { PG8_GREAD(vN, nxt, (ui + 1) & 1); } else { _Pragma("unroll") for (int h_ = 0; h_ < 2; ++h_) _Pragma("unroll") for (int i_ = 0; i_ < 2; ++i_) vN[h_][i_] = vC[h_][i_]; } } }
;             unsigned vS[2][2];
; #pragma unroll
;             for (int h_ = 0; h_ < 2; ++h_)
; #pragma unroll
;                 for (int i_ = 0; i_ < 2; ++i_) vS[h_][i_] = (GATHER && last) ? vN[h_][i_] : vC[h_][i_];
;             if constexpr (SP2) {
;             PG8_LDB(B0, 0, 0); PG8_LDB(B1, 0, 1); PG8_SCHED; PG8_LDA(At, 0, 0); PG8_STAGE(PG8_SA(1, 1), a1 + PG8_AH(1), PG8_VA(vC, 1));
;             PG8_WAIT_V(8); PG8_WAIT_L(0); PG8_BAR; PG8_MMA(0, 0, At, B0); PG8_MMA(0, 1, At, B1); PG8_BAR; PG8_SCHED;
;             PG8_LDA(At, 0, 1); PG8_STAGE(PG8_SB(0, 0), b2, voffB); PG8_STAGE(PG8_SB(0, 1), b2 + hstep, voffB); PG8_STAGE(PG8_SA(0, 0), a2, PG8_VA(vS, 0));
;             PG8_WAIT_V(8); PG8_WAIT_L(0); PG8_BAR; PG8_MMA(1, 0, At, B0); PG8_MMA(1, 1, At, B1); PG8_BAR; PG8_SCHED;
.LBB0_131:
	s_add_u32 s2, s8, 0xfffc0080
	s_addc_u32 s10, s9, -1
	s_cmp_eq_u32 s34, 12
	s_cselect_b32 s27, s21, s10
	s_cselect_b32 s26, s28, s2
	s_cselect_b32 s11, s19, s31
	s_cselect_b32 s10, s29, s30
	s_add_i32 s2, 0, 0x10000
	v_add_u32_e32 v0, s2, v143
	s_add_i32 s35, 0, 0x14000
	ds_read_b128 v[146:149], v0
	ds_read_b128 v[150:153], v0 offset:1024
	ds_read_b128 v[154:157], v0 offset:2048
	ds_read_b128 v[158:161], v0 offset:3072
	v_add_u32_e32 v0, s35, v143
	ds_read_b128 v[162:165], v0
	ds_read_b128 v[166:169], v0 offset:1024
	ds_read_b128 v[170:173], v0 offset:2048
	ds_read_b128 v[174:177], v0 offset:3072
	v_lshl_add_u64 v[210:211], s[8:9], 0, v[138:139]
	s_add_i32 m0, s46, 0xc000
	ds_read_b128 v[178:181], v145
	ds_read_b128 v[182:185], v145 offset:1024
	ds_read_b128 v[186:189], v145 offset:2048
	ds_read_b128 v[190:193], v145 offset:3072
	ds_read_b128 v[194:197], v145 offset:4096
	ds_read_b128 v[198:201], v145 offset:5120
	ds_read_b128 v[202:205], v145 offset:6144
	ds_read_b128 v[206:209], v145 offset:7168
	global_load_lds_dwordx4 v[210:211], off
	v_lshl_add_u64 v[210:211], s[8:9], 0, v[140:141]
	s_add_i32 m0, s46, 0xe000
	s_nop 0
	global_load_lds_dwordx4 v[210:211], off
	s_waitcnt vmcnt(8)
	s_waitcnt lgkmcnt(0)
	s_setprio 1
	s_barrier
	v_mfma_f32_16x16x32_bf16 v[126:129], v[146:149], v[178:181], v[126:129]
	v_mfma_f32_16x16x32_bf16 v[122:125], v[154:157], v[178:181], v[122:125]
	v_mfma_f32_16x16x32_bf16 v[118:121], v[146:149], v[186:189], v[118:121]
	v_mfma_f32_16x16x32_bf16 v[114:117], v[154:157], v[186:189], v[114:117]
	v_mfma_f32_16x16x32_bf16 v[110:113], v[146:149], v[194:197], v[110:113]
	v_mfma_f32_16x16x32_bf16 v[106:109], v[154:157], v[194:197], v[106:109]
	v_mfma_f32_16x16x32_bf16 v[102:105], v[146:149], v[202:205], v[102:105]
	v_mfma_f32_16x16x32_bf16 v[98:101], v[154:157], v[202:205], v[98:101]
	v_mfma_f32_16x16x32_bf16 v[126:129], v[150:153], v[182:185], v[126:129]
	v_mfma_f32_16x16x32_bf16 v[122:125], v[158:161], v[182:185], v[122:125]
	v_mfma_f32_16x16x32_bf16 v[118:121], v[150:153], v[190:193], v[118:121]
	v_mfma_f32_16x16x32_bf16 v[114:117], v[158:161], v[190:193], v[114:117]
	v_mfma_f32_16x16x32_bf16 v[110:113], v[150:153], v[198:201], v[110:113]
	v_mfma_f32_16x16x32_bf16 v[106:109], v[158:161], v[198:201], v[106:109]
	v_mfma_f32_16x16x32_bf16 v[102:105], v[150:153], v[206:209], v[102:105]
	v_mfma_f32_16x16x32_bf16 v[98:101], v[158:161], v[206:209], v[98:101]
	v_mfma_f32_16x16x32_bf16 v[62:65], v[162:165], v[178:181], v[62:65]
	v_mfma_f32_16x16x32_bf16 v[58:61], v[170:173], v[178:181], v[58:61]
	v_mfma_f32_16x16x32_bf16 v[54:57], v[162:165], v[186:189], v[54:57]
	v_mfma_f32_16x16x32_bf16 v[50:53], v[170:173], v[186:189], v[50:53]
	v_mfma_f32_16x16x32_bf16 v[46:49], v[162:165], v[194:197], v[46:49]
	v_mfma_f32_16x16x32_bf16 v[42:45], v[170:173], v[194:197], v[42:45]
	v_mfma_f32_16x16x32_bf16 v[38:41], v[162:165], v[202:205], v[38:41]
	v_mfma_f32_16x16x32_bf16 v[34:37], v[170:173], v[202:205], v[34:37]
	v_mfma_f32_16x16x32_bf16 v[62:65], v[166:169], v[182:185], v[62:65]
	v_mfma_f32_16x16x32_bf16 v[58:61], v[174:177], v[182:185], v[58:61]
	v_mfma_f32_16x16x32_bf16 v[54:57], v[166:169], v[190:193], v[54:57]
	v_mfma_f32_16x16x32_bf16 v[50:53], v[174:177], v[190:193], v[50:53]
	v_mfma_f32_16x16x32_bf16 v[46:49], v[166:169], v[198:201], v[46:49]
	v_mfma_f32_16x16x32_bf16 v[42:45], v[174:177], v[198:201], v[42:45]
	v_mfma_f32_16x16x32_bf16 v[38:41], v[166:169], v[206:209], v[38:41]
	v_mfma_f32_16x16x32_bf16 v[34:37], v[174:177], v[206:209], v[34:37]
	s_barrier
	s_setprio 0
	s_add_i32 s2, s2, s45
	v_lshl_add_u64 v[210:211], s[10:11], 0, v[134:135]
	s_mov_b32 m0, s2
	ds_read_b128 v[178:181], v145 offset:16384
	ds_read_b128 v[182:185], v145 offset:17408
	ds_read_b128 v[186:189], v145 offset:18432
	ds_read_b128 v[190:193], v145 offset:19456
	ds_read_b128 v[194:197], v145 offset:20480
	ds_read_b128 v[198:201], v145 offset:21504
	ds_read_b128 v[202:205], v145 offset:22528
	ds_read_b128 v[206:209], v145 offset:23552
	global_load_lds_dwordx4 v[210:211], off
	s_add_i32 m0, s2, 0x2000
	s_add_u32 s36, s10, 0x40000
	v_lshl_add_u64 v[212:213], s[10:11], 0, v[130:131]
	s_addc_u32 s37, s11, 0
	s_add_i32 s2, s35, s45
	global_load_lds_dwordx4 v[212:213], off
	v_lshl_add_u64 v[214:215], s[36:37], 0, v[134:135]
	s_mov_b32 m0, s2
	v_lshl_add_u64 v[216:217], s[26:27], 0, v[132:133]
	global_load_lds_dwordx4 v[214:215], off
	v_lshl_add_u64 v[214:215], s[36:37], 0, v[130:131]
	s_add_i32 m0, s2, 0x2000
	s_nop 0
	global_load_lds_dwordx4 v[214:215], off
	v_lshl_add_u64 v[214:215], s[26:27], 0, v[136:137]
	s_mov_b32 m0, s46
	s_nop 0
	global_load_lds_dwordx4 v[214:215], off
	s_mov_b32 m0, s47
	s_nop 0
	global_load_lds_dwordx4 v[216:217], off
	s_waitcnt vmcnt(8)
	s_waitcnt lgkmcnt(0)
	s_setprio 1
	s_barrier
; #define PG8_STAGE(bufoff, gbase, voff) do { _Pragma("unroll") for (int _i = 0; _i < 2; ++_i) \
;         __builtin_amdgcn_global_load_lds((const unsigned*)((const char*)(gbase) + (voff)[_i]), (PG8_LAS unsigned*)(lds + (bufoff) + ldsw + _i * 8192), 16, 0, 0); } while (0)
; #define PG8_LDA(dst, b, h) do { _Pragma("unroll") for (int m = 0; m < 4; ++m) _Pragma("unroll") for (int k = 0; k < 2; ++k) dst[m][k] = *(const PG8_LAS bf16x8*)(lds + PG8_SA(b, h) + aoff + m * 2048 + k * 1024); } while (0)
; #define PG8_LDB(dst, b, h) do { _Pragma("unroll") for (int n = 0; n < 2; ++n) _Pragma("unroll") for (int k = 0; k < 2; ++k) dst[n][k] = *(const PG8_LAS bf16x8*)(lds + PG8_SB(b, h) + boff + n * 2048 + k * 1024); } while (0)
; #define PG8_MMA(ai, bj, At, Bt) do { __builtin_amdgcn_s_setprio(1); _Pragma("unroll") for (int m = 0; m < 4; ++m) _Pragma("unroll") for (int n = 0; n < 2; ++n) _Pragma("unroll") for (int k = 0; k < 2; ++k) \
;         acc[ai][bj][m][n] = __builtin_amdgcn_mfma_f32_16x16x32_bf16(Bt[n][k], At[m][k], acc[ai][bj][m][n], 0, 0, 0); __builtin_amdgcn_s_setprio(0); } while (0)
; #define PG8_WAIT_V(n) asm volatile("s_waitcnt vmcnt(" #n ")" ::: "memory")
; #define PG8_WAIT_L(n) asm volatile("s_waitcnt lgkmcnt(" #n ")" ::: "memory")
; #define PG8_BAR __builtin_amdgcn_s_barrier()
; #define PG8_SCHED __builtin_amdgcn_sched_barrier(0)
; template <class Epi, class Sched, bool ALIGN_EPI = false, bool SP2 = false, bool GATHER = false>
; __device__ __forceinline__ void gemm_phase(PG8_LAS unsigned char* lds, const Gemm g, const Sched& S, const Epi& E, const int2* gslot = nullptr, PG8_LAS unsigned char* gtab = nullptr) {
;     ...
;             PG8_WAIT_V(8); PG8_WAIT_L(0); PG8_BAR; PG8_MMA(1, 0, At, B0); PG8_MMA(1, 1, At, B1); PG8_BAR; PG8_SCHED;
;             PG8_LDB(B0, 1, 0); PG8_LDB(B1, 1, 1); PG8_SCHED; PG8_LDA(At, 1, 0); PG8_STAGE(PG8_SA(0, 1), a2 + PG8_AH(1), PG8_VA(vS, 1));
;             PG8_WAIT_V(8); PG8_WAIT_L(0); PG8_BAR; PG8_MMA(0, 0, At, B0); PG8_MMA(0, 1, At, B1); PG8_BAR; PG8_SCHED;
	v_mfma_f32_16x16x32_bf16 v[94:97], v[146:149], v[178:181], v[94:97]
	v_mfma_f32_16x16x32_bf16 v[90:93], v[154:157], v[178:181], v[90:93]
	v_mfma_f32_16x16x32_bf16 v[86:89], v[146:149], v[186:189], v[86:89]
	v_mfma_f32_16x16x32_bf16 v[82:85], v[154:157], v[186:189], v[82:85]
	v_mfma_f32_16x16x32_bf16 v[78:81], v[146:149], v[194:197], v[78:81]
	v_mfma_f32_16x16x32_bf16 v[74:77], v[154:157], v[194:197], v[74:77]
	v_mfma_f32_16x16x32_bf16 v[70:73], v[146:149], v[202:205], v[70:73]
	v_mfma_f32_16x16x32_bf16 v[66:69], v[154:157], v[202:205], v[66:69]
	v_mfma_f32_16x16x32_bf16 v[94:97], v[150:153], v[182:185], v[94:97]
	v_mfma_f32_16x16x32_bf16 v[90:93], v[158:161], v[182:185], v[90:93]
	v_mfma_f32_16x16x32_bf16 v[86:89], v[150:153], v[190:193], v[86:89]
	v_mfma_f32_16x16x32_bf16 v[82:85], v[158:161], v[190:193], v[82:85]
	v_mfma_f32_16x16x32_bf16 v[78:81], v[150:153], v[198:201], v[78:81]
	v_mfma_f32_16x16x32_bf16 v[74:77], v[158:161], v[198:201], v[74:77]
	v_mfma_f32_16x16x32_bf16 v[70:73], v[150:153], v[206:209], v[70:73]
	v_mfma_f32_16x16x32_bf16 v[66:69], v[158:161], v[206:209], v[66:69]
	v_mfma_f32_16x16x32_bf16 v[30:33], v[162:165], v[178:181], v[30:33]
	v_mfma_f32_16x16x32_bf16 v[26:29], v[170:173], v[178:181], v[26:29]
	v_mfma_f32_16x16x32_bf16 v[22:25], v[162:165], v[186:189], v[22:25]
	v_mfma_f32_16x16x32_bf16 v[18:21], v[170:173], v[186:189], v[18:21]
	v_mfma_f32_16x16x32_bf16 v[14:17], v[162:165], v[194:197], v[14:17]
	v_mfma_f32_16x16x32_bf16 v[10:13], v[170:173], v[194:197], v[10:13]
	v_mfma_f32_16x16x32_bf16 v[6:9], v[162:165], v[202:205], v[6:9]
	v_mfma_f32_16x16x32_bf16 v[2:5], v[170:173], v[202:205], v[2:5]
	v_mfma_f32_16x16x32_bf16 v[30:33], v[166:169], v[182:185], v[30:33]
	v_mfma_f32_16x16x32_bf16 v[26:29], v[174:177], v[182:185], v[26:29]
	v_mfma_f32_16x16x32_bf16 v[22:25], v[166:169], v[190:193], v[22:25]
	v_mfma_f32_16x16x32_bf16 v[18:21], v[174:177], v[190:193], v[18:21]
	v_mfma_f32_16x16x32_bf16 v[14:17], v[166:169], v[198:201], v[14:17]
	v_mfma_f32_16x16x32_bf16 v[10:13], v[174:177], v[198:201], v[10:13]
	v_mfma_f32_16x16x32_bf16 v[6:9], v[166:169], v[206:209], v[6:9]
	v_mfma_f32_16x16x32_bf16 v[2:5], v[174:177], v[206:209], v[2:5]
	s_barrier
	s_setprio 0
	s_add_i32 s2, 0, 0x18000
	v_add_u32_e32 v0, s2, v143
	s_add_i32 s35, 0, 0x1c000
	ds_read_b128 v[146:149], v0
	ds_read_b128 v[150:153], v0 offset:1024
	ds_read_b128 v[154:157], v0 offset:2048
	ds_read_b128 v[158:161], v0 offset:3072
	v_add_u32_e32 v0, s35, v143
	ds_read_b128 v[162:165], v0
	ds_read_b128 v[166:169], v0 offset:1024
	ds_read_b128 v[170:173], v0 offset:2048
	ds_read_b128 v[174:177], v0 offset:3072
	s_add_u32 s26, s26, 0x40000
	s_addc_u32 s27, s27, 0
	s_mov_b32 m0, s50
	v_lshl_add_u64 v[218:219], s[26:27], 0, v[136:137]
	ds_read_b128 v[178:181], v145 offset:32768
	ds_read_b128 v[182:185], v145 offset:33792
	ds_read_b128 v[186:189], v145 offset:34816
	ds_read_b128 v[190:193], v145 offset:35840
	ds_read_b128 v[194:197], v145 offset:36864
	ds_read_b128 v[198:201], v145 offset:37888
	ds_read_b128 v[202:205], v145 offset:38912
	ds_read_b128 v[206:209], v145 offset:39936
	global_load_lds_dwordx4 v[218:219], off
	v_lshl_add_u64 v[218:219], s[26:27], 0, v[132:133]
	s_mov_b32 m0, s51
	s_nop 0
	global_load_lds_dwordx4 v[218:219], off
	s_waitcnt vmcnt(8)
	s_waitcnt lgkmcnt(0)
	s_setprio 1
	s_barrier
	v_mfma_f32_16x16x32_bf16 v[126:129], v[146:149], v[178:181], v[126:129]
	v_mfma_f32_16x16x32_bf16 v[122:125], v[154:157], v[178:181], v[122:125]
	v_mfma_f32_16x16x32_bf16 v[118:121], v[146:149], v[186:189], v[118:121]
	v_mfma_f32_16x16x32_bf16 v[114:117], v[154:157], v[186:189], v[114:117]
	v_mfma_f32_16x16x32_bf16 v[110:113], v[146:149], v[194:197], v[110:113]
	v_mfma_f32_16x16x32_bf16 v[106:109], v[154:157], v[194:197], v[106:109]
	v_mfma_f32_16x16x32_bf16 v[102:105], v[146:149], v[202:205], v[102:105]
	v_mfma_f32_16x16x32_bf16 v[98:101], v[154:157], v[202:205], v[98:101]
	v_mfma_f32_16x16x32_bf16 v[126:129], v[150:153], v[182:185], v[126:129]
	v_mfma_f32_16x16x32_bf16 v[122:125], v[158:161], v[182:185], v[122:125]
	v_mfma_f32_16x16x32_bf16 v[118:121], v[150:153], v[190:193], v[118:121]
	v_mfma_f32_16x16x32_bf16 v[114:117], v[158:161], v[190:193], v[114:117]
	v_mfma_f32_16x16x32_bf16 v[110:113], v[150:153], v[198:201], v[110:113]
	v_mfma_f32_16x16x32_bf16 v[106:109], v[158:161], v[198:201], v[106:109]
	v_mfma_f32_16x16x32_bf16 v[102:105], v[150:153], v[206:209], v[102:105]
	v_mfma_f32_16x16x32_bf16 v[98:101], v[158:161], v[206:209], v[98:101]
	v_mfma_f32_16x16x32_bf16 v[62:65], v[162:165], v[178:181], v[62:65]
	v_mfma_f32_16x16x32_bf16 v[58:61], v[170:173], v[178:181], v[58:61]
	v_mfma_f32_16x16x32_bf16 v[54:57], v[162:165], v[186:189], v[54:57]
	v_mfma_f32_16x16x32_bf16 v[50:53], v[170:173], v[186:189], v[50:53]
	v_mfma_f32_16x16x32_bf16 v[46:49], v[162:165], v[194:197], v[46:49]
	v_mfma_f32_16x16x32_bf16 v[42:45], v[170:173], v[194:197], v[42:45]
	v_mfma_f32_16x16x32_bf16 v[38:41], v[162:165], v[202:205], v[38:41]
	v_mfma_f32_16x16x32_bf16 v[34:37], v[170:173], v[202:205], v[34:37]
	v_mfma_f32_16x16x32_bf16 v[62:65], v[166:169], v[182:185], v[62:65]
	v_mfma_f32_16x16x32_bf16 v[58:61], v[174:177], v[182:185], v[58:61]
	v_mfma_f32_16x16x32_bf16 v[54:57], v[166:169], v[190:193], v[54:57]
	v_mfma_f32_16x16x32_bf16 v[50:53], v[174:177], v[190:193], v[50:53]
	v_mfma_f32_16x16x32_bf16 v[46:49], v[166:169], v[198:201], v[46:49]
	v_mfma_f32_16x16x32_bf16 v[42:45], v[174:177], v[198:201], v[42:45]
	v_mfma_f32_16x16x32_bf16 v[38:41], v[166:169], v[206:209], v[38:41]
	v_mfma_f32_16x16x32_bf16 v[34:37], v[174:177], v[206:209], v[34:37]
	s_barrier
; #define PG8_STAGE(bufoff, gbase, voff) do { _Pragma("unroll") for (int _i = 0; _i < 2; ++_i) \
;         __builtin_amdgcn_global_load_lds((const unsigned*)((const char*)(gbase) + (voff)[_i]), (PG8_LAS unsigned*)(lds + (bufoff) + ldsw + _i * 8192), 16, 0, 0); } while (0)
; #define PG8_LDA(dst, b, h) do { _Pragma("unroll") for (int m = 0; m < 4; ++m) _Pragma("unroll") for (int k = 0; k < 2; ++k) dst[m][k] = *(const PG8_LAS bf16x8*)(lds + PG8_SA(b, h) + aoff + m * 2048 + k * 1024); } while (0)
; #define PG8_MMA(ai, bj, At, Bt) do { __builtin_amdgcn_s_setprio(1); _Pragma("unroll") for (int m = 0; m < 4; ++m) _Pragma("unroll") for (int n = 0; n < 2; ++n) _Pragma("unroll") for (int k = 0; k < 2; ++k) \
;         acc[ai][bj][m][n] = __builtin_amdgcn_mfma_f32_16x16x32_bf16(Bt[n][k], At[m][k], acc[ai][bj][m][n], 0, 0, 0); __builtin_amdgcn_s_setprio(0); } while (0)
; #define PG8_WAIT_V(n) asm volatile("s_waitcnt vmcnt(" #n ")" ::: "memory")
; #define PG8_WAIT_L(n) asm volatile("s_waitcnt lgkmcnt(" #n ")" ::: "memory")
; #define PG8_BAR __builtin_amdgcn_s_barrier()
; #define PG8_SCHED __builtin_amdgcn_sched_barrier(0)
; template <class Epi, class Sched, bool ALIGN_EPI = false, bool SP2 = false, bool GATHER = false>
; __device__ __forceinline__ void gemm_phase(PG8_LAS unsigned char* lds, const Gemm g, const Sched& S, const Epi& E, const int2* gslot = nullptr, PG8_LAS unsigned char* gtab = nullptr) {
;     ...
;             PG8_LDA(At, 1, 1); PG8_STAGE(PG8_SB(1, 0), b3, voffB); PG8_STAGE(PG8_SB(1, 1), b3 + hstep, voffB); PG8_STAGE(PG8_SA(1, 0), a3, PG8_VA(vS, 0));
;             PG8_WAIT_V(8); PG8_WAIT_L(0); PG8_BAR; PG8_MMA(1, 0, At, B0); PG8_MMA(1, 1, At, B1); PG8_BAR; PG8_SCHED;
;     ...
;         if constexpr (ALIGN_EPI) { if (wr == 0) PG8_BAR; }
	s_setprio 0
	s_add_i32 s2, s2, s45
	v_lshl_add_u64 v[210:211], v[210:211], 0, s[54:55]
	s_mov_b32 m0, s2
	ds_read_b128 v[178:181], v145 offset:49152
	ds_read_b128 v[182:185], v145 offset:50176
	ds_read_b128 v[186:189], v145 offset:51200
	ds_read_b128 v[190:193], v145 offset:52224
	ds_read_b128 v[194:197], v145 offset:53248
	ds_read_b128 v[198:201], v145 offset:54272
	ds_read_b128 v[202:205], v145 offset:55296
	ds_read_b128 v[206:209], v145 offset:56320
	global_load_lds_dwordx4 v[210:211], off
	s_add_i32 m0, s2, 0x2000
	s_add_u32 s10, s10, 0x40080
	v_lshl_add_u64 v[210:211], v[212:213], 0, s[54:55]
	s_addc_u32 s11, s11, 0
	s_add_i32 s2, s35, s45
	global_load_lds_dwordx4 v[210:211], off
	v_lshl_add_u64 v[210:211], s[10:11], 0, v[134:135]
	s_mov_b32 m0, s2
	s_nop 0
	global_load_lds_dwordx4 v[210:211], off
	v_lshl_add_u64 v[210:211], s[10:11], 0, v[130:131]
	s_add_i32 m0, s2, 0x2000
	s_nop 0
	global_load_lds_dwordx4 v[210:211], off
	v_lshl_add_u64 v[210:211], v[214:215], 0, s[54:55]
	s_mov_b32 m0, s60
	s_nop 0
	global_load_lds_dwordx4 v[210:211], off
	v_lshl_add_u64 v[210:211], v[216:217], 0, s[54:55]
	s_mov_b32 m0, s61
	s_nop 0
	global_load_lds_dwordx4 v[210:211], off
	s_waitcnt vmcnt(8)
	s_waitcnt lgkmcnt(0)
	s_setprio 1
	s_barrier
	v_mfma_f32_16x16x32_bf16 v[94:97], v[146:149], v[178:181], v[94:97]
	v_mfma_f32_16x16x32_bf16 v[90:93], v[154:157], v[178:181], v[90:93]
	v_mfma_f32_16x16x32_bf16 v[86:89], v[146:149], v[186:189], v[86:89]
	v_mfma_f32_16x16x32_bf16 v[82:85], v[154:157], v[186:189], v[82:85]
	v_mfma_f32_16x16x32_bf16 v[78:81], v[146:149], v[194:197], v[78:81]
	v_mfma_f32_16x16x32_bf16 v[74:77], v[154:157], v[194:197], v[74:77]
	v_mfma_f32_16x16x32_bf16 v[70:73], v[146:149], v[202:205], v[70:73]
	v_mfma_f32_16x16x32_bf16 v[66:69], v[154:157], v[202:205], v[66:69]
	v_mfma_f32_16x16x32_bf16 v[94:97], v[150:153], v[182:185], v[94:97]
	v_mfma_f32_16x16x32_bf16 v[90:93], v[158:161], v[182:185], v[90:93]
	v_mfma_f32_16x16x32_bf16 v[86:89], v[150:153], v[190:193], v[86:89]
	v_mfma_f32_16x16x32_bf16 v[82:85], v[158:161], v[190:193], v[82:85]
	v_mfma_f32_16x16x32_bf16 v[78:81], v[150:153], v[198:201], v[78:81]
	v_mfma_f32_16x16x32_bf16 v[74:77], v[158:161], v[198:201], v[74:77]
	v_mfma_f32_16x16x32_bf16 v[70:73], v[150:153], v[206:209], v[70:73]
	v_mfma_f32_16x16x32_bf16 v[66:69], v[158:161], v[206:209], v[66:69]
	v_mfma_f32_16x16x32_bf16 v[30:33], v[162:165], v[178:181], v[30:33]
	v_mfma_f32_16x16x32_bf16 v[26:29], v[170:173], v[178:181], v[26:29]
	v_mfma_f32_16x16x32_bf16 v[22:25], v[162:165], v[186:189], v[22:25]
	v_mfma_f32_16x16x32_bf16 v[18:21], v[170:173], v[186:189], v[18:21]
	v_mfma_f32_16x16x32_bf16 v[14:17], v[162:165], v[194:197], v[14:17]
	v_mfma_f32_16x16x32_bf16 v[10:13], v[170:173], v[194:197], v[10:13]
	v_mfma_f32_16x16x32_bf16 v[6:9], v[162:165], v[202:205], v[6:9]
	v_mfma_f32_16x16x32_bf16 v[2:5], v[170:173], v[202:205], v[2:5]
	v_mfma_f32_16x16x32_bf16 v[30:33], v[166:169], v[182:185], v[30:33]
	v_mfma_f32_16x16x32_bf16 v[26:29], v[174:177], v[182:185], v[26:29]
	v_mfma_f32_16x16x32_bf16 v[22:25], v[166:169], v[190:193], v[22:25]
	v_mfma_f32_16x16x32_bf16 v[18:21], v[174:177], v[190:193], v[18:21]
	v_mfma_f32_16x16x32_bf16 v[14:17], v[166:169], v[198:201], v[14:17]
	v_mfma_f32_16x16x32_bf16 v[10:13], v[174:177], v[198:201], v[10:13]
	v_mfma_f32_16x16x32_bf16 v[6:9], v[166:169], v[206:209], v[6:9]
	v_mfma_f32_16x16x32_bf16 v[2:5], v[174:177], v[206:209], v[2:5]
	s_barrier
	s_setprio 0
	s_add_i32 s34, s34, 2
	s_add_u32 s8, s8, 0x100
	s_addc_u32 s9, s9, 0
	s_add_u32 s30, s30, 0x100
	s_addc_u32 s31, s31, 0
	s_cmp_gt_u32 s34, 13
	s_cbranch_scc0 .LBB0_131
	s_and_b64 vcc, exec, s[14:15]
	s_cbranch_vccz .LBB0_134
	s_barrier

; #define PG8_GREAD(dst, u, par) do { _Pragma("unroll") for (int h_ = 0; h_ < 2; ++h_) _Pragma("unroll") for (int i_ = 0; i_ < 2; ++i_) { const int rl_ = 128 * h_ + grl[i_]; \
;         const int tk_ = *(const PG8_LAS int*)(gtab + (par) * 2048 + rl_ * 8); const unsigned tok_ = (rl_ < (u).rows) ? ((unsigned)tk_ >> 2) : 0u; dst[h_][i_] = tok_ * (unsigned)(K * 2) + gcb[i_]; } } while (0)
; #define PG8_STAGE(bufoff, gbase, voff) do { _Pragma("unroll") for (int _i = 0; _i < 2; ++_i) \
;         __builtin_amdgcn_global_load_lds((const unsigned*)((const char*)(gbase) + (voff)[_i]), (PG8_LAS unsigned*)(lds + (bufoff) + ldsw + _i * 8192), 16, 0, 0); } while (0)
; #define PG8_WAIT_V(n) asm volatile("s_waitcnt vmcnt(" #n ")" ::: "memory")
; template <class Epi, class Sched, bool ALIGN_EPI = false, bool SP2 = false, bool GATHER = false>
; __device__ __forceinline__ void gemm_phase(PG8_LAS unsigned char* lds, const Gemm g, const Sched& S, const Epi& E, const int2* gslot = nullptr, PG8_LAS unsigned char* gtab = nullptr) {
;     ...
;             const char* a1 = cA + (size_t)(t + 1) * kstep;
;             const char* a2 = last ? nA : cA + (size_t)(t + 2) * kstep; const char* b2 = last ? nB : cB + (size_t)(t + 2) * kstep;
;             const char* a3 = a2 + kstep; const char* b3 = b2 + kstep;
;             if (last && has_next) S.a_ready(nxt);
;             if constexpr (GATHER) { if (last) { if (has_next) { PG8_GREAD(vN, nxt, (ui + 1) & 1); } else { _Pragma("unroll") for (int h_ = 0; h_ < 2; ++h_) _Pragma("unroll") for (int i_ = 0; i_ < 2; ++i_) vN[h_][i_] = vC[h_][i_]; } } }
;             unsigned vS[2][2];
; #pragma unroll
;             for (int h_ = 0; h_ < 2; ++h_)
; #pragma unroll
;                 for (int i_ = 0; i_ < 2; ++i_) vS[h_][i_] = (GATHER && last) ? vN[h_][i_] : vC[h_][i_];
;             if constexpr (SP2) {
;             PG8_LDB(B0, 0, 0); PG8_LDB(B1, 0, 1); PG8_SCHED; PG8_LDA(At, 0, 0); PG8_STAGE(PG8_SA(1, 1), a1 + PG8_AH(1), PG8_VA(vC, 1));
;             PG8_WAIT_V(8); PG8_WAIT_L(0); PG8_BAR; PG8_MMA(0, 0, At, B0); PG8_MMA(0, 1, At, B1); PG8_BAR; PG8_SCHED;
;             PG8_LDA(At, 0, 1); PG8_STAGE(PG8_SB(0, 0), b2, voffB); PG8_STAGE(PG8_SB(0, 1), b2 + hstep, voffB); PG8_STAGE(PG8_SA(0, 0), a2, PG8_VA(vS, 0));
;             PG8_WAIT_V(8); PG8_WAIT_L(0); PG8_BAR; PG8_MMA(1, 0, At, B0); PG8_MMA(1, 1, At, B1); PG8_BAR; PG8_SCHED;
.LBB0_482:
	s_add_u32 s34, s30, 0x100
	s_addc_u32 s35, s31, 0
	s_cmp_eq_u32 s66, 28
	s_cselect_b32 s39, s25, s35
	s_cselect_b32 s38, s62, s34
	s_cselect_b32 s37, s23, s65
	s_cselect_b32 s36, s63, s64
	s_add_i32 s2, 0, 0x10000
	s_add_i32 s67, 0, 0x14000
	v_add_u32_e32 v148, s2, v215
	v_add_u32_e32 v164, s67, v215
	ds_read_b128 v[136:139], v148
	ds_read_b128 v[140:143], v148 offset:1024
	ds_read_b128 v[144:147], v148 offset:2048
	ds_read_b128 v[148:151], v148 offset:3072
	ds_read_b128 v[152:155], v164
	ds_read_b128 v[156:159], v164 offset:1024
	ds_read_b128 v[160:163], v164 offset:2048
	ds_read_b128 v[164:167], v164 offset:3072
	v_lshl_add_u64 v[202:203], s[30:31], 0, v[132:133]
	s_add_i32 m0, s46, 0xc000
	ds_read_b128 v[168:171], v181
	ds_read_b128 v[172:175], v181 offset:1024
	ds_read_b128 v[176:179], v181 offset:2048
	ds_read_b128 v[182:185], v181 offset:3072
	ds_read_b128 v[186:189], v181 offset:4096
	ds_read_b128 v[190:193], v181 offset:5120
	ds_read_b128 v[194:197], v181 offset:6144
	ds_read_b128 v[198:201], v181 offset:7168
	global_load_lds_dwordx4 v[202:203], off
	v_lshl_add_u64 v[202:203], s[30:31], 0, v[134:135]
	s_add_i32 m0, s46, 0xe000
	s_nop 0
	global_load_lds_dwordx4 v[202:203], off
	s_waitcnt vmcnt(8)
	s_waitcnt lgkmcnt(0)
	s_setprio 1
	s_barrier
	v_mfma_f32_16x16x32_bf16 v[126:129], v[136:139], v[168:171], v[126:129]
	v_mfma_f32_16x16x32_bf16 v[122:125], v[144:147], v[168:171], v[122:125]
	v_mfma_f32_16x16x32_bf16 v[110:113], v[136:139], v[176:179], v[110:113]
	v_mfma_f32_16x16x32_bf16 v[106:109], v[144:147], v[176:179], v[106:109]
	v_mfma_f32_16x16x32_bf16 v[94:97], v[136:139], v[186:189], v[94:97]
	v_mfma_f32_16x16x32_bf16 v[90:93], v[144:147], v[186:189], v[90:93]
	v_mfma_f32_16x16x32_bf16 v[78:81], v[136:139], v[194:197], v[78:81]
	v_mfma_f32_16x16x32_bf16 v[74:77], v[144:147], v[194:197], v[74:77]
	v_mfma_f32_16x16x32_bf16 v[126:129], v[140:143], v[172:175], v[126:129]
	v_mfma_f32_16x16x32_bf16 v[122:125], v[148:151], v[172:175], v[122:125]
	v_mfma_f32_16x16x32_bf16 v[110:113], v[140:143], v[182:185], v[110:113]
	v_mfma_f32_16x16x32_bf16 v[106:109], v[148:151], v[182:185], v[106:109]
	v_mfma_f32_16x16x32_bf16 v[94:97], v[140:143], v[190:193], v[94:97]
	v_mfma_f32_16x16x32_bf16 v[90:93], v[148:151], v[190:193], v[90:93]
	v_mfma_f32_16x16x32_bf16 v[78:81], v[140:143], v[198:201], v[78:81]
	v_mfma_f32_16x16x32_bf16 v[74:77], v[148:151], v[198:201], v[74:77]
	v_mfma_f32_16x16x32_bf16 v[118:121], v[152:155], v[168:171], v[118:121]
	v_mfma_f32_16x16x32_bf16 v[114:117], v[160:163], v[168:171], v[114:117]
	v_mfma_f32_16x16x32_bf16 v[102:105], v[152:155], v[176:179], v[102:105]
	v_mfma_f32_16x16x32_bf16 v[98:101], v[160:163], v[176:179], v[98:101]
	v_mfma_f32_16x16x32_bf16 v[86:89], v[152:155], v[186:189], v[86:89]
	v_mfma_f32_16x16x32_bf16 v[82:85], v[160:163], v[186:189], v[82:85]
	v_mfma_f32_16x16x32_bf16 v[70:73], v[152:155], v[194:197], v[70:73]
	v_mfma_f32_16x16x32_bf16 v[66:69], v[160:163], v[194:197], v[66:69]
	v_mfma_f32_16x16x32_bf16 v[118:121], v[156:159], v[172:175], v[118:121]
	v_mfma_f32_16x16x32_bf16 v[114:117], v[164:167], v[172:175], v[114:117]
	v_mfma_f32_16x16x32_bf16 v[102:105], v[156:159], v[182:185], v[102:105]
	v_mfma_f32_16x16x32_bf16 v[98:101], v[164:167], v[182:185], v[98:101]
	v_mfma_f32_16x16x32_bf16 v[86:89], v[156:159], v[190:193], v[86:89]
	v_mfma_f32_16x16x32_bf16 v[82:85], v[164:167], v[190:193], v[82:85]
	v_mfma_f32_16x16x32_bf16 v[70:73], v[156:159], v[198:201], v[70:73]
	v_mfma_f32_16x16x32_bf16 v[66:69], v[164:167], v[198:201], v[66:69]
	s_barrier
	s_setprio 0
	s_add_i32 s2, s2, s45
	v_lshl_add_u64 v[202:203], s[36:37], 0, v[0:1]
	s_mov_b32 m0, s2
	ds_read_b128 v[168:171], v181 offset:16384
	ds_read_b128 v[172:175], v181 offset:17408
	ds_read_b128 v[176:179], v181 offset:18432
	ds_read_b128 v[182:185], v181 offset:19456
	ds_read_b128 v[186:189], v181 offset:20480
	ds_read_b128 v[190:193], v181 offset:21504
	ds_read_b128 v[194:197], v181 offset:22528
	ds_read_b128 v[198:201], v181 offset:23552
	global_load_lds_dwordx4 v[202:203], off
	s_add_i32 m0, s2, 0x2000
	s_add_u32 s30, s36, 0x80000
	v_lshl_add_u64 v[204:205], s[36:37], 0, v[130:131]
	s_addc_u32 s31, s37, 0
	s_add_i32 s2, s67, s45
	global_load_lds_dwordx4 v[204:205], off
	v_lshl_add_u64 v[206:207], s[30:31], 0, v[0:1]
	s_mov_b32 m0, s2
	v_lshl_add_u64 v[208:209], s[38:39], 0, v[130:131]
	global_load_lds_dwordx4 v[206:207], off
	v_lshl_add_u64 v[206:207], s[30:31], 0, v[130:131]
	s_add_i32 m0, s2, 0x2000
	s_nop 0
	global_load_lds_dwordx4 v[206:207], off
	v_lshl_add_u64 v[206:207], s[38:39], 0, v[0:1]
	s_mov_b32 m0, s46
	s_nop 0
	global_load_lds_dwordx4 v[206:207], off
	s_mov_b32 m0, s47
	s_nop 0
	global_load_lds_dwordx4 v[208:209], off
	s_waitcnt vmcnt(8)
	s_waitcnt lgkmcnt(0)
	s_setprio 1
	s_barrier
; #define PG8_STAGE(bufoff, gbase, voff) do { _Pragma("unroll") for (int _i = 0; _i < 2; ++_i) \
;         __builtin_amdgcn_global_load_lds((const unsigned*)((const char*)(gbase) + (voff)[_i]), (PG8_LAS unsigned*)(lds + (bufoff) + ldsw + _i * 8192), 16, 0, 0); } while (0)
; #define PG8_LDA(dst, b, h) do { _Pragma("unroll") for (int m = 0; m < 4; ++m) _Pragma("unroll") for (int k = 0; k < 2; ++k) dst[m][k] = *(const PG8_LAS bf16x8*)(lds + PG8_SA(b, h) + aoff + m * 2048 + k * 1024); } while (0)
; #define PG8_LDB(dst, b, h) do { _Pragma("unroll") for (int n = 0; n < 2; ++n) _Pragma("unroll") for (int k = 0; k < 2; ++k) dst[n][k] = *(const PG8_LAS bf16x8*)(lds + PG8_SB(b, h) + boff + n * 2048 + k * 1024); } while (0)
; #define PG8_MMA(ai, bj, At, Bt) do { __builtin_amdgcn_s_setprio(1); _Pragma("unroll") for (int m = 0; m < 4; ++m) _Pragma("unroll") for (int n = 0; n < 2; ++n) _Pragma("unroll") for (int k = 0; k < 2; ++k) \
;         acc[ai][bj][m][n] = __builtin_amdgcn_mfma_f32_16x16x32_bf16(Bt[n][k], At[m][k], acc[ai][bj][m][n], 0, 0, 0); __builtin_amdgcn_s_setprio(0); } while (0)
; #define PG8_WAIT_V(n) asm volatile("s_waitcnt vmcnt(" #n ")" ::: "memory")
; #define PG8_WAIT_L(n) asm volatile("s_waitcnt lgkmcnt(" #n ")" ::: "memory")
; #define PG8_BAR __builtin_amdgcn_s_barrier()
; #define PG8_SCHED __builtin_amdgcn_sched_barrier(0)
; template <class Epi, class Sched, bool ALIGN_EPI = false, bool SP2 = false, bool GATHER = false>
; __device__ __forceinline__ void gemm_phase(PG8_LAS unsigned char* lds, const Gemm g, const Sched& S, const Epi& E, const int2* gslot = nullptr, PG8_LAS unsigned char* gtab = nullptr) {
;     ...
;             PG8_WAIT_V(8); PG8_WAIT_L(0); PG8_BAR; PG8_MMA(1, 0, At, B0); PG8_MMA(1, 1, At, B1); PG8_BAR; PG8_SCHED;
;             PG8_LDB(B0, 1, 0); PG8_LDB(B1, 1, 1); PG8_SCHED; PG8_LDA(At, 1, 0); PG8_STAGE(PG8_SA(0, 1), a2 + PG8_AH(1), PG8_VA(vS, 1));
;             PG8_WAIT_V(8); PG8_WAIT_L(0); PG8_BAR; PG8_MMA(0, 0, At, B0); PG8_MMA(0, 1, At, B1); PG8_BAR; PG8_SCHED;
	v_mfma_f32_16x16x32_bf16 v[62:65], v[136:139], v[168:171], v[62:65]
	v_mfma_f32_16x16x32_bf16 v[58:61], v[144:147], v[168:171], v[58:61]
	v_mfma_f32_16x16x32_bf16 v[46:49], v[136:139], v[176:179], v[46:49]
	v_mfma_f32_16x16x32_bf16 v[42:45], v[144:147], v[176:179], v[42:45]
	v_mfma_f32_16x16x32_bf16 v[30:33], v[136:139], v[186:189], v[30:33]
	v_mfma_f32_16x16x32_bf16 v[26:29], v[144:147], v[186:189], v[26:29]
	v_mfma_f32_16x16x32_bf16 v[14:17], v[136:139], v[194:197], v[14:17]
	v_mfma_f32_16x16x32_bf16 v[10:13], v[144:147], v[194:197], v[10:13]
	v_mfma_f32_16x16x32_bf16 v[62:65], v[140:143], v[172:175], v[62:65]
	v_mfma_f32_16x16x32_bf16 v[58:61], v[148:151], v[172:175], v[58:61]
	v_mfma_f32_16x16x32_bf16 v[46:49], v[140:143], v[182:185], v[46:49]
	v_mfma_f32_16x16x32_bf16 v[42:45], v[148:151], v[182:185], v[42:45]
	v_mfma_f32_16x16x32_bf16 v[30:33], v[140:143], v[190:193], v[30:33]
	v_mfma_f32_16x16x32_bf16 v[26:29], v[148:151], v[190:193], v[26:29]
	v_mfma_f32_16x16x32_bf16 v[14:17], v[140:143], v[198:201], v[14:17]
	v_mfma_f32_16x16x32_bf16 v[10:13], v[148:151], v[198:201], v[10:13]
	v_mfma_f32_16x16x32_bf16 v[54:57], v[152:155], v[168:171], v[54:57]
	v_mfma_f32_16x16x32_bf16 v[50:53], v[160:163], v[168:171], v[50:53]
	v_mfma_f32_16x16x32_bf16 v[38:41], v[152:155], v[176:179], v[38:41]
	v_mfma_f32_16x16x32_bf16 v[34:37], v[160:163], v[176:179], v[34:37]
	v_mfma_f32_16x16x32_bf16 v[22:25], v[152:155], v[186:189], v[22:25]
	v_mfma_f32_16x16x32_bf16 v[18:21], v[160:163], v[186:189], v[18:21]
	v_mfma_f32_16x16x32_bf16 v[6:9], v[152:155], v[194:197], v[6:9]
	v_mfma_f32_16x16x32_bf16 v[2:5], v[160:163], v[194:197], v[2:5]
	v_mfma_f32_16x16x32_bf16 v[54:57], v[156:159], v[172:175], v[54:57]
	v_mfma_f32_16x16x32_bf16 v[50:53], v[164:167], v[172:175], v[50:53]
	v_mfma_f32_16x16x32_bf16 v[38:41], v[156:159], v[182:185], v[38:41]
	v_mfma_f32_16x16x32_bf16 v[34:37], v[164:167], v[182:185], v[34:37]
	v_mfma_f32_16x16x32_bf16 v[22:25], v[156:159], v[190:193], v[22:25]
	v_mfma_f32_16x16x32_bf16 v[18:21], v[164:167], v[190:193], v[18:21]
	v_mfma_f32_16x16x32_bf16 v[6:9], v[156:159], v[198:201], v[6:9]
	v_mfma_f32_16x16x32_bf16 v[2:5], v[164:167], v[198:201], v[2:5]
	s_barrier
	s_setprio 0
	s_add_i32 s2, 0, 0x18000
	s_add_i32 s67, 0, 0x1c000
	v_add_u32_e32 v148, s2, v215
	v_add_u32_e32 v164, s67, v215
	ds_read_b128 v[136:139], v148
	ds_read_b128 v[140:143], v148 offset:1024
	ds_read_b128 v[144:147], v148 offset:2048
	ds_read_b128 v[148:151], v148 offset:3072
	ds_read_b128 v[152:155], v164
	ds_read_b128 v[156:159], v164 offset:1024
	ds_read_b128 v[160:163], v164 offset:2048
	ds_read_b128 v[164:167], v164 offset:3072
	s_add_u32 s30, s38, 0x80000
	s_addc_u32 s31, s39, 0
	s_mov_b32 m0, s50
	v_lshl_add_u64 v[210:211], s[30:31], 0, v[0:1]
	ds_read_b128 v[168:171], v181 offset:32768
	ds_read_b128 v[172:175], v181 offset:33792
	ds_read_b128 v[176:179], v181 offset:34816
	ds_read_b128 v[182:185], v181 offset:35840
	ds_read_b128 v[186:189], v181 offset:36864
	ds_read_b128 v[190:193], v181 offset:37888
	ds_read_b128 v[194:197], v181 offset:38912
	ds_read_b128 v[198:201], v181 offset:39936
	global_load_lds_dwordx4 v[210:211], off
	v_lshl_add_u64 v[210:211], s[30:31], 0, v[130:131]
	s_mov_b32 m0, s51
	s_nop 0
	global_load_lds_dwordx4 v[210:211], off
	s_waitcnt vmcnt(8)
	s_waitcnt lgkmcnt(0)
	s_setprio 1
	s_barrier
	v_mfma_f32_16x16x32_bf16 v[126:129], v[136:139], v[168:171], v[126:129]
	v_mfma_f32_16x16x32_bf16 v[122:125], v[144:147], v[168:171], v[122:125]
	v_mfma_f32_16x16x32_bf16 v[110:113], v[136:139], v[176:179], v[110:113]
	v_mfma_f32_16x16x32_bf16 v[106:109], v[144:147], v[176:179], v[106:109]
	v_mfma_f32_16x16x32_bf16 v[94:97], v[136:139], v[186:189], v[94:97]
	v_mfma_f32_16x16x32_bf16 v[90:93], v[144:147], v[186:189], v[90:93]
	v_mfma_f32_16x16x32_bf16 v[78:81], v[136:139], v[194:197], v[78:81]
	v_mfma_f32_16x16x32_bf16 v[74:77], v[144:147], v[194:197], v[74:77]
	v_mfma_f32_16x16x32_bf16 v[126:129], v[140:143], v[172:175], v[126:129]
	v_mfma_f32_16x16x32_bf16 v[122:125], v[148:151], v[172:175], v[122:125]
	v_mfma_f32_16x16x32_bf16 v[110:113], v[140:143], v[182:185], v[110:113]
	v_mfma_f32_16x16x32_bf16 v[106:109], v[148:151], v[182:185], v[106:109]
	v_mfma_f32_16x16x32_bf16 v[94:97], v[140:143], v[190:193], v[94:97]
	v_mfma_f32_16x16x32_bf16 v[90:93], v[148:151], v[190:193], v[90:93]
	v_mfma_f32_16x16x32_bf16 v[78:81], v[140:143], v[198:201], v[78:81]
	v_mfma_f32_16x16x32_bf16 v[74:77], v[148:151], v[198:201], v[74:77]
	v_mfma_f32_16x16x32_bf16 v[118:121], v[152:155], v[168:171], v[118:121]
	v_mfma_f32_16x16x32_bf16 v[114:117], v[160:163], v[168:171], v[114:117]
	v_mfma_f32_16x16x32_bf16 v[102:105], v[152:155], v[176:179], v[102:105]
	v_mfma_f32_16x16x32_bf16 v[98:101], v[160:163], v[176:179], v[98:101]
	v_mfma_f32_16x16x32_bf16 v[86:89], v[152:155], v[186:189], v[86:89]
	v_mfma_f32_16x16x32_bf16 v[82:85], v[160:163], v[186:189], v[82:85]
	v_mfma_f32_16x16x32_bf16 v[70:73], v[152:155], v[194:197], v[70:73]
	v_mfma_f32_16x16x32_bf16 v[66:69], v[160:163], v[194:197], v[66:69]
	v_mfma_f32_16x16x32_bf16 v[118:121], v[156:159], v[172:175], v[118:121]
	v_mfma_f32_16x16x32_bf16 v[114:117], v[164:167], v[172:175], v[114:117]
	v_mfma_f32_16x16x32_bf16 v[102:105], v[156:159], v[182:185], v[102:105]
	v_mfma_f32_16x16x32_bf16 v[98:101], v[164:167], v[182:185], v[98:101]
	v_mfma_f32_16x16x32_bf16 v[86:89], v[156:159], v[190:193], v[86:89]
	v_mfma_f32_16x16x32_bf16 v[82:85], v[164:167], v[190:193], v[82:85]
	v_mfma_f32_16x16x32_bf16 v[70:73], v[156:159], v[198:201], v[70:73]
	v_mfma_f32_16x16x32_bf16 v[66:69], v[164:167], v[198:201], v[66:69]
	s_barrier
; #define PG8_STAGE(bufoff, gbase, voff) do { _Pragma("unroll") for (int _i = 0; _i < 2; ++_i) \
;         __builtin_amdgcn_global_load_lds((const unsigned*)((const char*)(gbase) + (voff)[_i]), (PG8_LAS unsigned*)(lds + (bufoff) + ldsw + _i * 8192), 16, 0, 0); } while (0)
; #define PG8_LDA(dst, b, h) do { _Pragma("unroll") for (int m = 0; m < 4; ++m) _Pragma("unroll") for (int k = 0; k < 2; ++k) dst[m][k] = *(const PG8_LAS bf16x8*)(lds + PG8_SA(b, h) + aoff + m * 2048 + k * 1024); } while (0)
; #define PG8_MMA(ai, bj, At, Bt) do { __builtin_amdgcn_s_setprio(1); _Pragma("unroll") for (int m = 0; m < 4; ++m) _Pragma("unroll") for (int n = 0; n < 2; ++n) _Pragma("unroll") for (int k = 0; k < 2; ++k) \
;         acc[ai][bj][m][n] = __builtin_amdgcn_mfma_f32_16x16x32_bf16(Bt[n][k], At[m][k], acc[ai][bj][m][n], 0, 0, 0); __builtin_amdgcn_s_setprio(0); } while (0)
; #define PG8_WAIT_V(n) asm volatile("s_waitcnt vmcnt(" #n ")" ::: "memory")
; #define PG8_WAIT_L(n) asm volatile("s_waitcnt lgkmcnt(" #n ")" ::: "memory")
; #define PG8_BAR __builtin_amdgcn_s_barrier()
; #define PG8_SCHED __builtin_amdgcn_sched_barrier(0)
; template <class Epi, class Sched, bool ALIGN_EPI = false, bool SP2 = false, bool GATHER = false>
; __device__ __forceinline__ void gemm_phase(PG8_LAS unsigned char* lds, const Gemm g, const Sched& S, const Epi& E, const int2* gslot = nullptr, PG8_LAS unsigned char* gtab = nullptr) {
;     ...
;             PG8_LDA(At, 1, 1); PG8_STAGE(PG8_SB(1, 0), b3, voffB); PG8_STAGE(PG8_SB(1, 1), b3 + hstep, voffB); PG8_STAGE(PG8_SA(1, 0), a3, PG8_VA(vS, 0));
;             PG8_WAIT_V(8); PG8_WAIT_L(0); PG8_BAR; PG8_MMA(1, 0, At, B0); PG8_MMA(1, 1, At, B1); PG8_BAR; PG8_SCHED;
;     ...
;         if constexpr (ALIGN_EPI) { if (wr == 0) PG8_BAR; }
	s_setprio 0
	s_add_i32 s2, s2, s45
	v_lshl_add_u64 v[202:203], v[202:203], 0, s[54:55]
	s_mov_b32 m0, s2
	ds_read_b128 v[168:171], v181 offset:49152
	ds_read_b128 v[172:175], v181 offset:50176
	ds_read_b128 v[176:179], v181 offset:51200
	ds_read_b128 v[182:185], v181 offset:52224
	ds_read_b128 v[186:189], v181 offset:53248
	ds_read_b128 v[190:193], v181 offset:54272
	ds_read_b128 v[194:197], v181 offset:55296
	ds_read_b128 v[198:201], v181 offset:56320
	global_load_lds_dwordx4 v[202:203], off
	s_add_i32 m0, s2, 0x2000
	s_add_u32 s30, s36, 0x80080
	v_lshl_add_u64 v[202:203], v[204:205], 0, s[54:55]
	s_addc_u32 s31, s37, 0
	s_add_i32 s2, s67, s45
	global_load_lds_dwordx4 v[202:203], off
	v_lshl_add_u64 v[202:203], s[30:31], 0, v[0:1]
	s_mov_b32 m0, s2
	s_nop 0
	global_load_lds_dwordx4 v[202:203], off
	v_lshl_add_u64 v[202:203], s[30:31], 0, v[130:131]
	s_add_i32 m0, s2, 0x2000
	s_nop 0
	global_load_lds_dwordx4 v[202:203], off
	v_lshl_add_u64 v[202:203], v[206:207], 0, s[54:55]
	s_mov_b32 m0, s52
	s_nop 0
	global_load_lds_dwordx4 v[202:203], off
	v_lshl_add_u64 v[202:203], v[208:209], 0, s[54:55]
	s_mov_b32 m0, s53
	s_nop 0
	global_load_lds_dwordx4 v[202:203], off
	s_waitcnt vmcnt(8)
	s_waitcnt lgkmcnt(0)
	s_setprio 1
	s_barrier
	v_mfma_f32_16x16x32_bf16 v[62:65], v[136:139], v[168:171], v[62:65]
	v_mfma_f32_16x16x32_bf16 v[58:61], v[144:147], v[168:171], v[58:61]
	v_mfma_f32_16x16x32_bf16 v[46:49], v[136:139], v[176:179], v[46:49]
	v_mfma_f32_16x16x32_bf16 v[42:45], v[144:147], v[176:179], v[42:45]
	v_mfma_f32_16x16x32_bf16 v[30:33], v[136:139], v[186:189], v[30:33]
	v_mfma_f32_16x16x32_bf16 v[26:29], v[144:147], v[186:189], v[26:29]
	v_mfma_f32_16x16x32_bf16 v[14:17], v[136:139], v[194:197], v[14:17]
	v_mfma_f32_16x16x32_bf16 v[10:13], v[144:147], v[194:197], v[10:13]
	v_mfma_f32_16x16x32_bf16 v[62:65], v[140:143], v[172:175], v[62:65]
	v_mfma_f32_16x16x32_bf16 v[58:61], v[148:151], v[172:175], v[58:61]
	v_mfma_f32_16x16x32_bf16 v[46:49], v[140:143], v[182:185], v[46:49]
	v_mfma_f32_16x16x32_bf16 v[42:45], v[148:151], v[182:185], v[42:45]
	v_mfma_f32_16x16x32_bf16 v[30:33], v[140:143], v[190:193], v[30:33]
	v_mfma_f32_16x16x32_bf16 v[26:29], v[148:151], v[190:193], v[26:29]
	v_mfma_f32_16x16x32_bf16 v[14:17], v[140:143], v[198:201], v[14:17]
	v_mfma_f32_16x16x32_bf16 v[10:13], v[148:151], v[198:201], v[10:13]
	v_mfma_f32_16x16x32_bf16 v[54:57], v[152:155], v[168:171], v[54:57]
	v_mfma_f32_16x16x32_bf16 v[50:53], v[160:163], v[168:171], v[50:53]
	v_mfma_f32_16x16x32_bf16 v[38:41], v[152:155], v[176:179], v[38:41]
	v_mfma_f32_16x16x32_bf16 v[34:37], v[160:163], v[176:179], v[34:37]
	v_mfma_f32_16x16x32_bf16 v[22:25], v[152:155], v[186:189], v[22:25]
	v_mfma_f32_16x16x32_bf16 v[18:21], v[160:163], v[186:189], v[18:21]
	v_mfma_f32_16x16x32_bf16 v[6:9], v[152:155], v[194:197], v[6:9]
	v_mfma_f32_16x16x32_bf16 v[2:5], v[160:163], v[194:197], v[2:5]
	v_mfma_f32_16x16x32_bf16 v[54:57], v[156:159], v[172:175], v[54:57]
	v_mfma_f32_16x16x32_bf16 v[50:53], v[164:167], v[172:175], v[50:53]
	v_mfma_f32_16x16x32_bf16 v[38:41], v[156:159], v[182:185], v[38:41]
	v_mfma_f32_16x16x32_bf16 v[34:37], v[164:167], v[182:185], v[34:37]
	v_mfma_f32_16x16x32_bf16 v[22:25], v[156:159], v[190:193], v[22:25]
	v_mfma_f32_16x16x32_bf16 v[18:21], v[164:167], v[190:193], v[18:21]
	v_mfma_f32_16x16x32_bf16 v[6:9], v[156:159], v[198:201], v[6:9]
	v_mfma_f32_16x16x32_bf16 v[2:5], v[164:167], v[198:201], v[2:5]
	s_barrier
	s_setprio 0
	s_add_i32 s66, s66, 2
	s_add_u32 s64, s64, 0x100
	s_addc_u32 s65, s65, 0
	s_cmp_gt_u32 s66, 29
	s_mov_b64 s[30:31], s[34:35]
	s_cbranch_scc0 .LBB0_482
	s_and_b64 vcc, exec, s[20:21]
	s_cbranch_vccz .LBB0_485
	s_barrier

; #define PG8_GREAD(dst, u, par) do { _Pragma("unroll") for (int h_ = 0; h_ < 2; ++h_) _Pragma("unroll") for (int i_ = 0; i_ < 2; ++i_) { const int rl_ = 128 * h_ + grl[i_]; \
;         const int tk_ = *(const PG8_LAS int*)(gtab + (par) * 2048 + rl_ * 8); const unsigned tok_ = (rl_ < (u).rows) ? ((unsigned)tk_ >> 2) : 0u; dst[h_][i_] = tok_ * (unsigned)(K * 2) + gcb[i_]; } } while (0)
; #define PG8_STAGE(bufoff, gbase, voff) do { _Pragma("unroll") for (int _i = 0; _i < 2; ++_i) \
;         __builtin_amdgcn_global_load_lds((const unsigned*)((const char*)(gbase) + (voff)[_i]), (PG8_LAS unsigned*)(lds + (bufoff) + ldsw + _i * 8192), 16, 0, 0); } while (0)
; #define PG8_WAIT_V(n) asm volatile("s_waitcnt vmcnt(" #n ")" ::: "memory")
; template <class Epi, class Sched, bool ALIGN_EPI = false, bool SP2 = false, bool GATHER = false>
; __device__ __forceinline__ void gemm_phase(PG8_LAS unsigned char* lds, const Gemm g, const Sched& S, const Epi& E, const int2* gslot = nullptr, PG8_LAS unsigned char* gtab = nullptr) {
;     ...
;             const char* a1 = cA + (size_t)(t + 1) * kstep;
;             const char* a2 = last ? nA : cA + (size_t)(t + 2) * kstep; const char* b2 = last ? nB : cB + (size_t)(t + 2) * kstep;
;             const char* a3 = a2 + kstep; const char* b3 = b2 + kstep;
;             if (last && has_next) S.a_ready(nxt);
;             if constexpr (GATHER) { if (last) { if (has_next) { PG8_GREAD(vN, nxt, (ui + 1) & 1); } else { _Pragma("unroll") for (int h_ = 0; h_ < 2; ++h_) _Pragma("unroll") for (int i_ = 0; i_ < 2; ++i_) vN[h_][i_] = vC[h_][i_]; } } }
;             unsigned vS[2][2];
; #pragma unroll
;             for (int h_ = 0; h_ < 2; ++h_)
; #pragma unroll
;                 for (int i_ = 0; i_ < 2; ++i_) vS[h_][i_] = (GATHER && last) ? vN[h_][i_] : vC[h_][i_];
;             if constexpr (SP2) {
;             PG8_LDB(B0, 0, 0); PG8_LDB(B1, 0, 1); PG8_SCHED; PG8_LDA(At, 0, 0); PG8_STAGE(PG8_SA(1, 1), a1 + PG8_AH(1), PG8_VA(vC, 1));
;             PG8_WAIT_V(8); PG8_WAIT_L(0); PG8_BAR; PG8_MMA(0, 0, At, B0); PG8_MMA(0, 1, At, B1); PG8_BAR; PG8_SCHED;
;             PG8_LDA(At, 0, 1); PG8_STAGE(PG8_SB(0, 0), b2, voffB); PG8_STAGE(PG8_SB(0, 1), b2 + hstep, voffB); PG8_STAGE(PG8_SA(0, 0), a2, PG8_VA(vS, 0));
;             PG8_WAIT_V(8); PG8_WAIT_L(0); PG8_BAR; PG8_MMA(1, 0, At, B0); PG8_MMA(1, 1, At, B1); PG8_BAR; PG8_SCHED;
.LBB0_565:
	s_add_u32 s2, s24, 0xfffc0080
	s_addc_u32 s26, s25, -1
	s_cmp_eq_u32 s62, 12
	s_cselect_b32 s29, s19, s26
	s_cselect_b32 s28, s53, s2
	s_cselect_b32 s27, s15, s61
	s_cselect_b32 s26, s56, s60
	s_add_i32 s2, 0, 0x10000
	v_add_u32_e32 v140, s2, v146
	s_add_i32 s63, 0, 0x14000
	ds_read_b128 v[142:145], v140
	ds_read_b128 v[150:153], v140 offset:1024
	ds_read_b128 v[154:157], v140 offset:2048
	ds_read_b128 v[158:161], v140 offset:3072
	v_add_u32_e32 v140, s63, v146
	ds_read_b128 v[162:165], v140
	ds_read_b128 v[166:169], v140 offset:1024
	ds_read_b128 v[170:173], v140 offset:2048
	ds_read_b128 v[174:177], v140 offset:3072
	v_lshl_add_u64 v[210:211], s[24:25], 0, v[136:137]
	s_add_i32 m0, s36, 0xc000
	ds_read_b128 v[178:181], v148
	ds_read_b128 v[182:185], v148 offset:1024
	ds_read_b128 v[186:189], v148 offset:2048
	ds_read_b128 v[190:193], v148 offset:3072
	ds_read_b128 v[194:197], v148 offset:4096
	ds_read_b128 v[198:201], v148 offset:5120
	ds_read_b128 v[202:205], v148 offset:6144
	ds_read_b128 v[206:209], v148 offset:7168
	global_load_lds_dwordx4 v[210:211], off
	v_lshl_add_u64 v[210:211], s[24:25], 0, v[138:139]
	s_add_i32 m0, s36, 0xe000
	s_nop 0
	global_load_lds_dwordx4 v[210:211], off
	s_waitcnt vmcnt(8)
	s_waitcnt lgkmcnt(0)
	s_setprio 1
	s_barrier
	v_mfma_f32_16x16x32_bf16 v[126:129], v[142:145], v[178:181], v[126:129]
	v_mfma_f32_16x16x32_bf16 v[122:125], v[154:157], v[178:181], v[122:125]
	v_mfma_f32_16x16x32_bf16 v[114:117], v[142:145], v[186:189], v[114:117]
	v_mfma_f32_16x16x32_bf16 v[106:109], v[154:157], v[186:189], v[106:109]
	v_mfma_f32_16x16x32_bf16 v[98:101], v[142:145], v[194:197], v[98:101]
	v_mfma_f32_16x16x32_bf16 v[90:93], v[154:157], v[194:197], v[90:93]
	v_mfma_f32_16x16x32_bf16 v[82:85], v[142:145], v[202:205], v[82:85]
	v_mfma_f32_16x16x32_bf16 v[74:77], v[154:157], v[202:205], v[74:77]
	v_mfma_f32_16x16x32_bf16 v[126:129], v[150:153], v[182:185], v[126:129]
	v_mfma_f32_16x16x32_bf16 v[122:125], v[158:161], v[182:185], v[122:125]
	v_mfma_f32_16x16x32_bf16 v[114:117], v[150:153], v[190:193], v[114:117]
	v_mfma_f32_16x16x32_bf16 v[106:109], v[158:161], v[190:193], v[106:109]
	v_mfma_f32_16x16x32_bf16 v[98:101], v[150:153], v[198:201], v[98:101]
	v_mfma_f32_16x16x32_bf16 v[90:93], v[158:161], v[198:201], v[90:93]
	v_mfma_f32_16x16x32_bf16 v[82:85], v[150:153], v[206:209], v[82:85]
	v_mfma_f32_16x16x32_bf16 v[74:77], v[158:161], v[206:209], v[74:77]
	v_mfma_f32_16x16x32_bf16 v[118:121], v[162:165], v[178:181], v[118:121]
	v_mfma_f32_16x16x32_bf16 v[110:113], v[170:173], v[178:181], v[110:113]
	v_mfma_f32_16x16x32_bf16 v[102:105], v[162:165], v[186:189], v[102:105]
	v_mfma_f32_16x16x32_bf16 v[94:97], v[170:173], v[186:189], v[94:97]
	v_mfma_f32_16x16x32_bf16 v[86:89], v[162:165], v[194:197], v[86:89]
	v_mfma_f32_16x16x32_bf16 v[78:81], v[170:173], v[194:197], v[78:81]
	v_mfma_f32_16x16x32_bf16 v[70:73], v[162:165], v[202:205], v[70:73]
	v_mfma_f32_16x16x32_bf16 v[66:69], v[170:173], v[202:205], v[66:69]
	v_mfma_f32_16x16x32_bf16 v[118:121], v[166:169], v[182:185], v[118:121]
	v_mfma_f32_16x16x32_bf16 v[110:113], v[174:177], v[182:185], v[110:113]
	v_mfma_f32_16x16x32_bf16 v[102:105], v[166:169], v[190:193], v[102:105]
	v_mfma_f32_16x16x32_bf16 v[94:97], v[174:177], v[190:193], v[94:97]
	v_mfma_f32_16x16x32_bf16 v[86:89], v[166:169], v[198:201], v[86:89]
	v_mfma_f32_16x16x32_bf16 v[78:81], v[174:177], v[198:201], v[78:81]
	v_mfma_f32_16x16x32_bf16 v[70:73], v[166:169], v[206:209], v[70:73]
	v_mfma_f32_16x16x32_bf16 v[66:69], v[174:177], v[206:209], v[66:69]
	s_barrier
	s_setprio 0
	s_add_i32 s2, s2, s35
	v_lshl_add_u64 v[210:211], s[26:27], 0, v[0:1]
	s_mov_b32 m0, s2
	ds_read_b128 v[178:181], v148 offset:16384
	ds_read_b128 v[182:185], v148 offset:17408
	ds_read_b128 v[186:189], v148 offset:18432
	ds_read_b128 v[190:193], v148 offset:19456
	ds_read_b128 v[194:197], v148 offset:20480
	ds_read_b128 v[198:201], v148 offset:21504
	ds_read_b128 v[202:205], v148 offset:22528
	ds_read_b128 v[206:209], v148 offset:23552
	global_load_lds_dwordx4 v[210:211], off
	s_add_i32 m0, s2, 0x2000
	s_add_u32 s64, s26, 0x40000
	v_lshl_add_u64 v[212:213], s[26:27], 0, v[130:131]
	s_addc_u32 s65, s27, 0
	s_add_i32 s2, s63, s35
	global_load_lds_dwordx4 v[212:213], off
	v_lshl_add_u64 v[214:215], s[64:65], 0, v[0:1]
	s_mov_b32 m0, s2
	v_lshl_add_u64 v[216:217], s[28:29], 0, v[132:133]
	global_load_lds_dwordx4 v[214:215], off
	v_lshl_add_u64 v[214:215], s[64:65], 0, v[130:131]
	s_add_i32 m0, s2, 0x2000
	s_nop 0
	global_load_lds_dwordx4 v[214:215], off
	v_lshl_add_u64 v[214:215], s[28:29], 0, v[134:135]
	s_mov_b32 m0, s36
	s_nop 0
	global_load_lds_dwordx4 v[214:215], off
	s_mov_b32 m0, s37
	s_nop 0
	global_load_lds_dwordx4 v[216:217], off
	s_waitcnt vmcnt(8)
	s_waitcnt lgkmcnt(0)
	s_setprio 1
	s_barrier
; #define PG8_STAGE(bufoff, gbase, voff) do { _Pragma("unroll") for (int _i = 0; _i < 2; ++_i) \
;         __builtin_amdgcn_global_load_lds((const unsigned*)((const char*)(gbase) + (voff)[_i]), (PG8_LAS unsigned*)(lds + (bufoff) + ldsw + _i * 8192), 16, 0, 0); } while (0)
; #define PG8_LDA(dst, b, h) do { _Pragma("unroll") for (int m = 0; m < 4; ++m) _Pragma("unroll") for (int k = 0; k < 2; ++k) dst[m][k] = *(const PG8_LAS bf16x8*)(lds + PG8_SA(b, h) + aoff + m * 2048 + k * 1024); } while (0)
; #define PG8_LDB(dst, b, h) do { _Pragma("unroll") for (int n = 0; n < 2; ++n) _Pragma("unroll") for (int k = 0; k < 2; ++k) dst[n][k] = *(const PG8_LAS bf16x8*)(lds + PG8_SB(b, h) + boff + n * 2048 + k * 1024); } while (0)
; #define PG8_MMA(ai, bj, At, Bt) do { __builtin_amdgcn_s_setprio(1); _Pragma("unroll") for (int m = 0; m < 4; ++m) _Pragma("unroll") for (int n = 0; n < 2; ++n) _Pragma("unroll") for (int k = 0; k < 2; ++k) \
;         acc[ai][bj][m][n] = __builtin_amdgcn_mfma_f32_16x16x32_bf16(Bt[n][k], At[m][k], acc[ai][bj][m][n], 0, 0, 0); __builtin_amdgcn_s_setprio(0); } while (0)
; #define PG8_WAIT_V(n) asm volatile("s_waitcnt vmcnt(" #n ")" ::: "memory")
; #define PG8_WAIT_L(n) asm volatile("s_waitcnt lgkmcnt(" #n ")" ::: "memory")
; #define PG8_BAR __builtin_amdgcn_s_barrier()
; #define PG8_SCHED __builtin_amdgcn_sched_barrier(0)
; template <class Epi, class Sched, bool ALIGN_EPI = false, bool SP2 = false, bool GATHER = false>
; __device__ __forceinline__ void gemm_phase(PG8_LAS unsigned char* lds, const Gemm g, const Sched& S, const Epi& E, const int2* gslot = nullptr, PG8_LAS unsigned char* gtab = nullptr) {
;     ...
;             PG8_WAIT_V(8); PG8_WAIT_L(0); PG8_BAR; PG8_MMA(1, 0, At, B0); PG8_MMA(1, 1, At, B1); PG8_BAR; PG8_SCHED;
;             PG8_LDB(B0, 1, 0); PG8_LDB(B1, 1, 1); PG8_SCHED; PG8_LDA(At, 1, 0); PG8_STAGE(PG8_SA(0, 1), a2 + PG8_AH(1), PG8_VA(vS, 1));
;             PG8_WAIT_V(8); PG8_WAIT_L(0); PG8_BAR; PG8_MMA(0, 0, At, B0); PG8_MMA(0, 1, At, B1); PG8_BAR; PG8_SCHED;
	v_mfma_f32_16x16x32_bf16 v[62:65], v[142:145], v[178:181], v[62:65]
	v_mfma_f32_16x16x32_bf16 v[58:61], v[154:157], v[178:181], v[58:61]
	v_mfma_f32_16x16x32_bf16 v[50:53], v[142:145], v[186:189], v[50:53]
	v_mfma_f32_16x16x32_bf16 v[42:45], v[154:157], v[186:189], v[42:45]
	v_mfma_f32_16x16x32_bf16 v[34:37], v[142:145], v[194:197], v[34:37]
	v_mfma_f32_16x16x32_bf16 v[26:29], v[154:157], v[194:197], v[26:29]
	v_mfma_f32_16x16x32_bf16 v[18:21], v[142:145], v[202:205], v[18:21]
	v_mfma_f32_16x16x32_bf16 v[10:13], v[154:157], v[202:205], v[10:13]
	v_mfma_f32_16x16x32_bf16 v[62:65], v[150:153], v[182:185], v[62:65]
	v_mfma_f32_16x16x32_bf16 v[58:61], v[158:161], v[182:185], v[58:61]
	v_mfma_f32_16x16x32_bf16 v[50:53], v[150:153], v[190:193], v[50:53]
	v_mfma_f32_16x16x32_bf16 v[42:45], v[158:161], v[190:193], v[42:45]
	v_mfma_f32_16x16x32_bf16 v[34:37], v[150:153], v[198:201], v[34:37]
	v_mfma_f32_16x16x32_bf16 v[26:29], v[158:161], v[198:201], v[26:29]
	v_mfma_f32_16x16x32_bf16 v[18:21], v[150:153], v[206:209], v[18:21]
	v_mfma_f32_16x16x32_bf16 v[10:13], v[158:161], v[206:209], v[10:13]
	v_mfma_f32_16x16x32_bf16 v[54:57], v[162:165], v[178:181], v[54:57]
	v_mfma_f32_16x16x32_bf16 v[46:49], v[170:173], v[178:181], v[46:49]
	v_mfma_f32_16x16x32_bf16 v[38:41], v[162:165], v[186:189], v[38:41]
	v_mfma_f32_16x16x32_bf16 v[30:33], v[170:173], v[186:189], v[30:33]
	v_mfma_f32_16x16x32_bf16 v[22:25], v[162:165], v[194:197], v[22:25]
	v_mfma_f32_16x16x32_bf16 v[14:17], v[170:173], v[194:197], v[14:17]
	v_mfma_f32_16x16x32_bf16 v[6:9], v[162:165], v[202:205], v[6:9]
	v_mfma_f32_16x16x32_bf16 v[2:5], v[170:173], v[202:205], v[2:5]
	v_mfma_f32_16x16x32_bf16 v[54:57], v[166:169], v[182:185], v[54:57]
	v_mfma_f32_16x16x32_bf16 v[46:49], v[174:177], v[182:185], v[46:49]
	v_mfma_f32_16x16x32_bf16 v[38:41], v[166:169], v[190:193], v[38:41]
	v_mfma_f32_16x16x32_bf16 v[30:33], v[174:177], v[190:193], v[30:33]
	v_mfma_f32_16x16x32_bf16 v[22:25], v[166:169], v[198:201], v[22:25]
	v_mfma_f32_16x16x32_bf16 v[14:17], v[174:177], v[198:201], v[14:17]
	v_mfma_f32_16x16x32_bf16 v[6:9], v[166:169], v[206:209], v[6:9]
	v_mfma_f32_16x16x32_bf16 v[2:5], v[174:177], v[206:209], v[2:5]
	s_barrier
	s_setprio 0
	s_add_i32 s2, 0, 0x18000
	v_add_u32_e32 v140, s2, v146
	s_add_i32 s63, 0, 0x1c000
	ds_read_b128 v[142:145], v140
	ds_read_b128 v[150:153], v140 offset:1024
	ds_read_b128 v[154:157], v140 offset:2048
	ds_read_b128 v[158:161], v140 offset:3072
	v_add_u32_e32 v140, s63, v146
	ds_read_b128 v[162:165], v140
	ds_read_b128 v[166:169], v140 offset:1024
	ds_read_b128 v[170:173], v140 offset:2048
	ds_read_b128 v[174:177], v140 offset:3072
	s_add_u32 s28, s28, 0x40000
	s_addc_u32 s29, s29, 0
	s_mov_b32 m0, s38
	v_lshl_add_u64 v[218:219], s[28:29], 0, v[134:135]
	ds_read_b128 v[178:181], v148 offset:32768
	ds_read_b128 v[182:185], v148 offset:33792
	ds_read_b128 v[186:189], v148 offset:34816
	ds_read_b128 v[190:193], v148 offset:35840
	ds_read_b128 v[194:197], v148 offset:36864
	ds_read_b128 v[198:201], v148 offset:37888
	ds_read_b128 v[202:205], v148 offset:38912
	ds_read_b128 v[206:209], v148 offset:39936
	global_load_lds_dwordx4 v[218:219], off
	v_lshl_add_u64 v[218:219], s[28:29], 0, v[132:133]
	s_mov_b32 m0, s39
	s_nop 0
	global_load_lds_dwordx4 v[218:219], off
	s_waitcnt vmcnt(8)
	s_waitcnt lgkmcnt(0)
	s_setprio 1
	s_barrier
	v_mfma_f32_16x16x32_bf16 v[126:129], v[142:145], v[178:181], v[126:129]
	v_mfma_f32_16x16x32_bf16 v[122:125], v[154:157], v[178:181], v[122:125]
	v_mfma_f32_16x16x32_bf16 v[114:117], v[142:145], v[186:189], v[114:117]
	v_mfma_f32_16x16x32_bf16 v[106:109], v[154:157], v[186:189], v[106:109]
	v_mfma_f32_16x16x32_bf16 v[98:101], v[142:145], v[194:197], v[98:101]
	v_mfma_f32_16x16x32_bf16 v[90:93], v[154:157], v[194:197], v[90:93]
	v_mfma_f32_16x16x32_bf16 v[82:85], v[142:145], v[202:205], v[82:85]
	v_mfma_f32_16x16x32_bf16 v[74:77], v[154:157], v[202:205], v[74:77]
	v_mfma_f32_16x16x32_bf16 v[126:129], v[150:153], v[182:185], v[126:129]
	v_mfma_f32_16x16x32_bf16 v[122:125], v[158:161], v[182:185], v[122:125]
	v_mfma_f32_16x16x32_bf16 v[114:117], v[150:153], v[190:193], v[114:117]
	v_mfma_f32_16x16x32_bf16 v[106:109], v[158:161], v[190:193], v[106:109]
	v_mfma_f32_16x16x32_bf16 v[98:101], v[150:153], v[198:201], v[98:101]
	v_mfma_f32_16x16x32_bf16 v[90:93], v[158:161], v[198:201], v[90:93]
	v_mfma_f32_16x16x32_bf16 v[82:85], v[150:153], v[206:209], v[82:85]
	v_mfma_f32_16x16x32_bf16 v[74:77], v[158:161], v[206:209], v[74:77]
	v_mfma_f32_16x16x32_bf16 v[118:121], v[162:165], v[178:181], v[118:121]
	v_mfma_f32_16x16x32_bf16 v[110:113], v[170:173], v[178:181], v[110:113]
	v_mfma_f32_16x16x32_bf16 v[102:105], v[162:165], v[186:189], v[102:105]
	v_mfma_f32_16x16x32_bf16 v[94:97], v[170:173], v[186:189], v[94:97]
	v_mfma_f32_16x16x32_bf16 v[86:89], v[162:165], v[194:197], v[86:89]
	v_mfma_f32_16x16x32_bf16 v[78:81], v[170:173], v[194:197], v[78:81]
	v_mfma_f32_16x16x32_bf16 v[70:73], v[162:165], v[202:205], v[70:73]
	v_mfma_f32_16x16x32_bf16 v[66:69], v[170:173], v[202:205], v[66:69]
	v_mfma_f32_16x16x32_bf16 v[118:121], v[166:169], v[182:185], v[118:121]
	v_mfma_f32_16x16x32_bf16 v[110:113], v[174:177], v[182:185], v[110:113]
	v_mfma_f32_16x16x32_bf16 v[102:105], v[166:169], v[190:193], v[102:105]
	v_mfma_f32_16x16x32_bf16 v[94:97], v[174:177], v[190:193], v[94:97]
	v_mfma_f32_16x16x32_bf16 v[86:89], v[166:169], v[198:201], v[86:89]
	v_mfma_f32_16x16x32_bf16 v[78:81], v[174:177], v[198:201], v[78:81]
	v_mfma_f32_16x16x32_bf16 v[70:73], v[166:169], v[206:209], v[70:73]
	v_mfma_f32_16x16x32_bf16 v[66:69], v[174:177], v[206:209], v[66:69]
	s_barrier
; #define PG8_STAGE(bufoff, gbase, voff) do { _Pragma("unroll") for (int _i = 0; _i < 2; ++_i) \
;         __builtin_amdgcn_global_load_lds((const unsigned*)((const char*)(gbase) + (voff)[_i]), (PG8_LAS unsigned*)(lds + (bufoff) + ldsw + _i * 8192), 16, 0, 0); } while (0)
; #define PG8_LDA(dst, b, h) do { _Pragma("unroll") for (int m = 0; m < 4; ++m) _Pragma("unroll") for (int k = 0; k < 2; ++k) dst[m][k] = *(const PG8_LAS bf16x8*)(lds + PG8_SA(b, h) + aoff + m * 2048 + k * 1024); } while (0)
; #define PG8_MMA(ai, bj, At, Bt) do { __builtin_amdgcn_s_setprio(1); _Pragma("unroll") for (int m = 0; m < 4; ++m) _Pragma("unroll") for (int n = 0; n < 2; ++n) _Pragma("unroll") for (int k = 0; k < 2; ++k) \
;         acc[ai][bj][m][n] = __builtin_amdgcn_mfma_f32_16x16x32_bf16(Bt[n][k], At[m][k], acc[ai][bj][m][n], 0, 0, 0); __builtin_amdgcn_s_setprio(0); } while (0)
; #define PG8_WAIT_V(n) asm volatile("s_waitcnt vmcnt(" #n ")" ::: "memory")
; #define PG8_WAIT_L(n) asm volatile("s_waitcnt lgkmcnt(" #n ")" ::: "memory")
; #define PG8_BAR __builtin_amdgcn_s_barrier()
; #define PG8_SCHED __builtin_amdgcn_sched_barrier(0)
; template <class Epi, class Sched, bool ALIGN_EPI = false, bool SP2 = false, bool GATHER = false>
; __device__ __forceinline__ void gemm_phase(PG8_LAS unsigned char* lds, const Gemm g, const Sched& S, const Epi& E, const int2* gslot = nullptr, PG8_LAS unsigned char* gtab = nullptr) {
;     ...
;             PG8_LDA(At, 1, 1); PG8_STAGE(PG8_SB(1, 0), b3, voffB); PG8_STAGE(PG8_SB(1, 1), b3 + hstep, voffB); PG8_STAGE(PG8_SA(1, 0), a3, PG8_VA(vS, 0));
;             PG8_WAIT_V(8); PG8_WAIT_L(0); PG8_BAR; PG8_MMA(1, 0, At, B0); PG8_MMA(1, 1, At, B1); PG8_BAR; PG8_SCHED;
;     ...
;         if constexpr (ALIGN_EPI) { if (wr == 0) PG8_BAR; }
	s_setprio 0
	s_add_i32 s2, s2, s35
	v_lshl_add_u64 v[210:211], v[210:211], 0, s[54:55]
	s_mov_b32 m0, s2
	ds_read_b128 v[178:181], v148 offset:49152
	ds_read_b128 v[182:185], v148 offset:50176
	ds_read_b128 v[186:189], v148 offset:51200
	ds_read_b128 v[190:193], v148 offset:52224
	ds_read_b128 v[194:197], v148 offset:53248
	ds_read_b128 v[198:201], v148 offset:54272
	ds_read_b128 v[202:205], v148 offset:55296
	ds_read_b128 v[206:209], v148 offset:56320
	global_load_lds_dwordx4 v[210:211], off
	s_add_i32 m0, s2, 0x2000
	s_add_u32 s26, s26, 0x40080
	v_lshl_add_u64 v[210:211], v[212:213], 0, s[54:55]
	s_addc_u32 s27, s27, 0
	s_add_i32 s2, s63, s35
	global_load_lds_dwordx4 v[210:211], off
	v_lshl_add_u64 v[210:211], s[26:27], 0, v[0:1]
	s_mov_b32 m0, s2
	s_nop 0
	global_load_lds_dwordx4 v[210:211], off
	v_lshl_add_u64 v[210:211], s[26:27], 0, v[130:131]
	s_add_i32 m0, s2, 0x2000
	s_nop 0
	global_load_lds_dwordx4 v[210:211], off
	v_lshl_add_u64 v[210:211], v[214:215], 0, s[54:55]
	s_mov_b32 m0, s44
	s_nop 0
	global_load_lds_dwordx4 v[210:211], off
	v_lshl_add_u64 v[210:211], v[216:217], 0, s[54:55]
	s_mov_b32 m0, s45
	s_nop 0
	global_load_lds_dwordx4 v[210:211], off
	s_waitcnt vmcnt(8)
	s_waitcnt lgkmcnt(0)
	s_setprio 1
	s_barrier
	v_mfma_f32_16x16x32_bf16 v[62:65], v[142:145], v[178:181], v[62:65]
	v_mfma_f32_16x16x32_bf16 v[58:61], v[154:157], v[178:181], v[58:61]
	v_mfma_f32_16x16x32_bf16 v[50:53], v[142:145], v[186:189], v[50:53]
	v_mfma_f32_16x16x32_bf16 v[42:45], v[154:157], v[186:189], v[42:45]
	v_mfma_f32_16x16x32_bf16 v[34:37], v[142:145], v[194:197], v[34:37]
	v_mfma_f32_16x16x32_bf16 v[26:29], v[154:157], v[194:197], v[26:29]
	v_mfma_f32_16x16x32_bf16 v[18:21], v[142:145], v[202:205], v[18:21]
	v_mfma_f32_16x16x32_bf16 v[10:13], v[154:157], v[202:205], v[10:13]
	v_mfma_f32_16x16x32_bf16 v[62:65], v[150:153], v[182:185], v[62:65]
	v_mfma_f32_16x16x32_bf16 v[58:61], v[158:161], v[182:185], v[58:61]
	v_mfma_f32_16x16x32_bf16 v[50:53], v[150:153], v[190:193], v[50:53]
	v_mfma_f32_16x16x32_bf16 v[42:45], v[158:161], v[190:193], v[42:45]
	v_mfma_f32_16x16x32_bf16 v[34:37], v[150:153], v[198:201], v[34:37]
	v_mfma_f32_16x16x32_bf16 v[26:29], v[158:161], v[198:201], v[26:29]
	v_mfma_f32_16x16x32_bf16 v[18:21], v[150:153], v[206:209], v[18:21]
	v_mfma_f32_16x16x32_bf16 v[10:13], v[158:161], v[206:209], v[10:13]
	v_mfma_f32_16x16x32_bf16 v[54:57], v[162:165], v[178:181], v[54:57]
	v_mfma_f32_16x16x32_bf16 v[46:49], v[170:173], v[178:181], v[46:49]
	v_mfma_f32_16x16x32_bf16 v[38:41], v[162:165], v[186:189], v[38:41]
	v_mfma_f32_16x16x32_bf16 v[30:33], v[170:173], v[186:189], v[30:33]
	v_mfma_f32_16x16x32_bf16 v[22:25], v[162:165], v[194:197], v[22:25]
	v_mfma_f32_16x16x32_bf16 v[14:17], v[170:173], v[194:197], v[14:17]
	v_mfma_f32_16x16x32_bf16 v[6:9], v[162:165], v[202:205], v[6:9]
	v_mfma_f32_16x16x32_bf16 v[2:5], v[170:173], v[202:205], v[2:5]
	v_mfma_f32_16x16x32_bf16 v[54:57], v[166:169], v[182:185], v[54:57]
	v_mfma_f32_16x16x32_bf16 v[46:49], v[174:177], v[182:185], v[46:49]
	v_mfma_f32_16x16x32_bf16 v[38:41], v[166:169], v[190:193], v[38:41]
	v_mfma_f32_16x16x32_bf16 v[30:33], v[174:177], v[190:193], v[30:33]
	v_mfma_f32_16x16x32_bf16 v[22:25], v[166:169], v[198:201], v[22:25]
	v_mfma_f32_16x16x32_bf16 v[14:17], v[174:177], v[198:201], v[14:17]
	v_mfma_f32_16x16x32_bf16 v[6:9], v[166:169], v[206:209], v[6:9]
	v_mfma_f32_16x16x32_bf16 v[2:5], v[174:177], v[206:209], v[2:5]
	s_barrier
	s_setprio 0
	s_add_i32 s62, s62, 2
	s_add_u32 s24, s24, 0x100
	s_addc_u32 s25, s25, 0
	s_add_u32 s60, s60, 0x100
	s_addc_u32 s61, s61, 0
	s_cmp_gt_u32 s62, 13
	s_cbranch_scc0 .LBB0_565
	s_and_b64 vcc, exec, s[12:13]
	s_cbranch_vccz .LBB0_568
	s_barrier

; #define PG8_GREAD(dst, u, par) do { _Pragma("unroll") for (int h_ = 0; h_ < 2; ++h_) _Pragma("unroll") for (int i_ = 0; i_ < 2; ++i_) { const int rl_ = 128 * h_ + grl[i_]; \
;         const int tk_ = *(const PG8_LAS int*)(gtab + (par) * 2048 + rl_ * 8); const unsigned tok_ = (rl_ < (u).rows) ? ((unsigned)tk_ >> 2) : 0u; dst[h_][i_] = tok_ * (unsigned)(K * 2) + gcb[i_]; } } while (0)
; #define PG8_STAGE(bufoff, gbase, voff) do { _Pragma("unroll") for (int _i = 0; _i < 2; ++_i) \
;         __builtin_amdgcn_global_load_lds((const unsigned*)((const char*)(gbase) + (voff)[_i]), (PG8_LAS unsigned*)(lds + (bufoff) + ldsw + _i * 8192), 16, 0, 0); } while (0)
; #define PG8_WAIT_V(n) asm volatile("s_waitcnt vmcnt(" #n ")" ::: "memory")
; template <class Epi, class Sched, bool ALIGN_EPI = false, bool SP2 = false, bool GATHER = false>
; __device__ __forceinline__ void gemm_phase(PG8_LAS unsigned char* lds, const Gemm g, const Sched& S, const Epi& E, const int2* gslot = nullptr, PG8_LAS unsigned char* gtab = nullptr) {
;     ...
;             const char* a1 = cA + (size_t)(t + 1) * kstep;
;             const char* a2 = last ? nA : cA + (size_t)(t + 2) * kstep; const char* b2 = last ? nB : cB + (size_t)(t + 2) * kstep;
;             const char* a3 = a2 + kstep; const char* b3 = b2 + kstep;
;             if (last && has_next) S.a_ready(nxt);
;             if constexpr (GATHER) { if (last) { if (has_next) { PG8_GREAD(vN, nxt, (ui + 1) & 1); } else { _Pragma("unroll") for (int h_ = 0; h_ < 2; ++h_) _Pragma("unroll") for (int i_ = 0; i_ < 2; ++i_) vN[h_][i_] = vC[h_][i_]; } } }
;             unsigned vS[2][2];
; #pragma unroll
;             for (int h_ = 0; h_ < 2; ++h_)
; #pragma unroll
;                 for (int i_ = 0; i_ < 2; ++i_) vS[h_][i_] = (GATHER && last) ? vN[h_][i_] : vC[h_][i_];
;             if constexpr (SP2) {
;             PG8_LDB(B0, 0, 0); PG8_LDB(B1, 0, 1); PG8_SCHED; PG8_LDA(At, 0, 0); PG8_STAGE(PG8_SA(1, 1), a1 + PG8_AH(1), PG8_VA(vC, 1));
;             PG8_WAIT_V(8); PG8_WAIT_L(0); PG8_BAR; PG8_MMA(0, 0, At, B0); PG8_MMA(0, 1, At, B1); PG8_BAR; PG8_SCHED;
;             PG8_LDA(At, 0, 1); PG8_STAGE(PG8_SB(0, 0), b2, voffB); PG8_STAGE(PG8_SB(0, 1), b2 + hstep, voffB); PG8_STAGE(PG8_SA(0, 0), a2, PG8_VA(vS, 0));
;             PG8_WAIT_V(8); PG8_WAIT_L(0); PG8_BAR; PG8_MMA(1, 0, At, B0); PG8_MMA(1, 1, At, B1); PG8_BAR; PG8_SCHED;
.LBB0_813:
	s_add_u32 s30, s28, 0x100
	s_addc_u32 s31, s29, 0
	s_cmp_eq_u32 s63, 12
	s_cselect_b32 s37, s23, s31
	s_cselect_b32 s36, s59, s30
	s_cselect_b32 s35, s21, s62
	s_cselect_b32 s34, s60, s61
	s_add_i32 s2, 0, 0x10000
	s_add_i32 s64, 0, 0x14000
	v_add_u32_e32 v148, s2, v215
	v_add_u32_e32 v164, s64, v215
	ds_read_b128 v[136:139], v148
	ds_read_b128 v[140:143], v148 offset:1024
	ds_read_b128 v[144:147], v148 offset:2048
	ds_read_b128 v[148:151], v148 offset:3072
	ds_read_b128 v[152:155], v164
	ds_read_b128 v[156:159], v164 offset:1024
	ds_read_b128 v[160:163], v164 offset:2048
	ds_read_b128 v[164:167], v164 offset:3072
	v_lshl_add_u64 v[202:203], s[28:29], 0, v[132:133]
	s_add_i32 m0, s44, 0xc000
	ds_read_b128 v[168:171], v181
	ds_read_b128 v[172:175], v181 offset:1024
	ds_read_b128 v[176:179], v181 offset:2048
	ds_read_b128 v[182:185], v181 offset:3072
	ds_read_b128 v[186:189], v181 offset:4096
	ds_read_b128 v[190:193], v181 offset:5120
	ds_read_b128 v[194:197], v181 offset:6144
	ds_read_b128 v[198:201], v181 offset:7168
	global_load_lds_dwordx4 v[202:203], off
	v_lshl_add_u64 v[202:203], s[28:29], 0, v[134:135]
	s_add_i32 m0, s44, 0xe000
	s_nop 0
	global_load_lds_dwordx4 v[202:203], off
	s_waitcnt vmcnt(8)
	s_waitcnt lgkmcnt(0)
	s_setprio 1
	s_barrier
	v_mfma_f32_16x16x32_bf16 v[126:129], v[136:139], v[168:171], v[126:129]
	v_mfma_f32_16x16x32_bf16 v[122:125], v[144:147], v[168:171], v[122:125]
	v_mfma_f32_16x16x32_bf16 v[110:113], v[136:139], v[176:179], v[110:113]
	v_mfma_f32_16x16x32_bf16 v[106:109], v[144:147], v[176:179], v[106:109]
	v_mfma_f32_16x16x32_bf16 v[94:97], v[136:139], v[186:189], v[94:97]
	v_mfma_f32_16x16x32_bf16 v[90:93], v[144:147], v[186:189], v[90:93]
	v_mfma_f32_16x16x32_bf16 v[78:81], v[136:139], v[194:197], v[78:81]
	v_mfma_f32_16x16x32_bf16 v[74:77], v[144:147], v[194:197], v[74:77]
	v_mfma_f32_16x16x32_bf16 v[126:129], v[140:143], v[172:175], v[126:129]
	v_mfma_f32_16x16x32_bf16 v[122:125], v[148:151], v[172:175], v[122:125]
	v_mfma_f32_16x16x32_bf16 v[110:113], v[140:143], v[182:185], v[110:113]
	v_mfma_f32_16x16x32_bf16 v[106:109], v[148:151], v[182:185], v[106:109]
	v_mfma_f32_16x16x32_bf16 v[94:97], v[140:143], v[190:193], v[94:97]
	v_mfma_f32_16x16x32_bf16 v[90:93], v[148:151], v[190:193], v[90:93]
	v_mfma_f32_16x16x32_bf16 v[78:81], v[140:143], v[198:201], v[78:81]
	v_mfma_f32_16x16x32_bf16 v[74:77], v[148:151], v[198:201], v[74:77]
	v_mfma_f32_16x16x32_bf16 v[118:121], v[152:155], v[168:171], v[118:121]
	v_mfma_f32_16x16x32_bf16 v[114:117], v[160:163], v[168:171], v[114:117]
	v_mfma_f32_16x16x32_bf16 v[102:105], v[152:155], v[176:179], v[102:105]
	v_mfma_f32_16x16x32_bf16 v[98:101], v[160:163], v[176:179], v[98:101]
	v_mfma_f32_16x16x32_bf16 v[86:89], v[152:155], v[186:189], v[86:89]
	v_mfma_f32_16x16x32_bf16 v[82:85], v[160:163], v[186:189], v[82:85]
	v_mfma_f32_16x16x32_bf16 v[70:73], v[152:155], v[194:197], v[70:73]
	v_mfma_f32_16x16x32_bf16 v[66:69], v[160:163], v[194:197], v[66:69]
	v_mfma_f32_16x16x32_bf16 v[118:121], v[156:159], v[172:175], v[118:121]
	v_mfma_f32_16x16x32_bf16 v[114:117], v[164:167], v[172:175], v[114:117]
	v_mfma_f32_16x16x32_bf16 v[102:105], v[156:159], v[182:185], v[102:105]
	v_mfma_f32_16x16x32_bf16 v[98:101], v[164:167], v[182:185], v[98:101]
	v_mfma_f32_16x16x32_bf16 v[86:89], v[156:159], v[190:193], v[86:89]
	v_mfma_f32_16x16x32_bf16 v[82:85], v[164:167], v[190:193], v[82:85]
	v_mfma_f32_16x16x32_bf16 v[70:73], v[156:159], v[198:201], v[70:73]
	v_mfma_f32_16x16x32_bf16 v[66:69], v[164:167], v[198:201], v[66:69]
	s_barrier
	s_setprio 0
	s_add_i32 s2, s2, s43
	v_lshl_add_u64 v[202:203], s[34:35], 0, v[0:1]
	s_mov_b32 m0, s2
	ds_read_b128 v[168:171], v181 offset:16384
	ds_read_b128 v[172:175], v181 offset:17408
	ds_read_b128 v[176:179], v181 offset:18432
	ds_read_b128 v[182:185], v181 offset:19456
	ds_read_b128 v[186:189], v181 offset:20480
	ds_read_b128 v[190:193], v181 offset:21504
	ds_read_b128 v[194:197], v181 offset:22528
	ds_read_b128 v[198:201], v181 offset:23552
	global_load_lds_dwordx4 v[202:203], off
	s_add_i32 m0, s2, 0x2000
	s_add_u32 s28, s34, 0x40000
	v_lshl_add_u64 v[204:205], s[34:35], 0, v[130:131]
	s_addc_u32 s29, s35, 0
	s_add_i32 s2, s64, s43
	global_load_lds_dwordx4 v[204:205], off
	v_lshl_add_u64 v[206:207], s[28:29], 0, v[0:1]
	s_mov_b32 m0, s2
	v_lshl_add_u64 v[208:209], s[36:37], 0, v[130:131]
	global_load_lds_dwordx4 v[206:207], off
	v_lshl_add_u64 v[206:207], s[28:29], 0, v[130:131]
	s_add_i32 m0, s2, 0x2000
	s_nop 0
	global_load_lds_dwordx4 v[206:207], off
	v_lshl_add_u64 v[206:207], s[36:37], 0, v[0:1]
	s_mov_b32 m0, s44
	s_nop 0
	global_load_lds_dwordx4 v[206:207], off
	s_mov_b32 m0, s45
	s_nop 0
	global_load_lds_dwordx4 v[208:209], off
	s_waitcnt vmcnt(8)
	s_waitcnt lgkmcnt(0)
	s_setprio 1
	s_barrier
; #define PG8_STAGE(bufoff, gbase, voff) do { _Pragma("unroll") for (int _i = 0; _i < 2; ++_i) \
;         __builtin_amdgcn_global_load_lds((const unsigned*)((const char*)(gbase) + (voff)[_i]), (PG8_LAS unsigned*)(lds + (bufoff) + ldsw + _i * 8192), 16, 0, 0); } while (0)
; #define PG8_LDA(dst, b, h) do { _Pragma("unroll") for (int m = 0; m < 4; ++m) _Pragma("unroll") for (int k = 0; k < 2; ++k) dst[m][k] = *(const PG8_LAS bf16x8*)(lds + PG8_SA(b, h) + aoff + m * 2048 + k * 1024); } while (0)
; #define PG8_LDB(dst, b, h) do { _Pragma("unroll") for (int n = 0; n < 2; ++n) _Pragma("unroll") for (int k = 0; k < 2; ++k) dst[n][k] = *(const PG8_LAS bf16x8*)(lds + PG8_SB(b, h) + boff + n * 2048 + k * 1024); } while (0)
; #define PG8_MMA(ai, bj, At, Bt) do { __builtin_amdgcn_s_setprio(1); _Pragma("unroll") for (int m = 0; m < 4; ++m) _Pragma("unroll") for (int n = 0; n < 2; ++n) _Pragma("unroll") for (int k = 0; k < 2; ++k) \
;         acc[ai][bj][m][n] = __builtin_amdgcn_mfma_f32_16x16x32_bf16(Bt[n][k], At[m][k], acc[ai][bj][m][n], 0, 0, 0); __builtin_amdgcn_s_setprio(0); } while (0)
; #define PG8_WAIT_V(n) asm volatile("s_waitcnt vmcnt(" #n ")" ::: "memory")
; #define PG8_WAIT_L(n) asm volatile("s_waitcnt lgkmcnt(" #n ")" ::: "memory")
; #define PG8_BAR __builtin_amdgcn_s_barrier()
; #define PG8_SCHED __builtin_amdgcn_sched_barrier(0)
; template <class Epi, class Sched, bool ALIGN_EPI = false, bool SP2 = false, bool GATHER = false>
; __device__ __forceinline__ void gemm_phase(PG8_LAS unsigned char* lds, const Gemm g, const Sched& S, const Epi& E, const int2* gslot = nullptr, PG8_LAS unsigned char* gtab = nullptr) {
;     ...
;             PG8_WAIT_V(8); PG8_WAIT_L(0); PG8_BAR; PG8_MMA(1, 0, At, B0); PG8_MMA(1, 1, At, B1); PG8_BAR; PG8_SCHED;
;             PG8_LDB(B0, 1, 0); PG8_LDB(B1, 1, 1); PG8_SCHED; PG8_LDA(At, 1, 0); PG8_STAGE(PG8_SA(0, 1), a2 + PG8_AH(1), PG8_VA(vS, 1));
;             PG8_WAIT_V(8); PG8_WAIT_L(0); PG8_BAR; PG8_MMA(0, 0, At, B0); PG8_MMA(0, 1, At, B1); PG8_BAR; PG8_SCHED;
	v_mfma_f32_16x16x32_bf16 v[62:65], v[136:139], v[168:171], v[62:65]
	v_mfma_f32_16x16x32_bf16 v[58:61], v[144:147], v[168:171], v[58:61]
	v_mfma_f32_16x16x32_bf16 v[46:49], v[136:139], v[176:179], v[46:49]
	v_mfma_f32_16x16x32_bf16 v[42:45], v[144:147], v[176:179], v[42:45]
	v_mfma_f32_16x16x32_bf16 v[30:33], v[136:139], v[186:189], v[30:33]
	v_mfma_f32_16x16x32_bf16 v[26:29], v[144:147], v[186:189], v[26:29]
	v_mfma_f32_16x16x32_bf16 v[14:17], v[136:139], v[194:197], v[14:17]
	v_mfma_f32_16x16x32_bf16 v[10:13], v[144:147], v[194:197], v[10:13]
	v_mfma_f32_16x16x32_bf16 v[62:65], v[140:143], v[172:175], v[62:65]
	v_mfma_f32_16x16x32_bf16 v[58:61], v[148:151], v[172:175], v[58:61]
	v_mfma_f32_16x16x32_bf16 v[46:49], v[140:143], v[182:185], v[46:49]
	v_mfma_f32_16x16x32_bf16 v[42:45], v[148:151], v[182:185], v[42:45]
	v_mfma_f32_16x16x32_bf16 v[30:33], v[140:143], v[190:193], v[30:33]
	v_mfma_f32_16x16x32_bf16 v[26:29], v[148:151], v[190:193], v[26:29]
	v_mfma_f32_16x16x32_bf16 v[14:17], v[140:143], v[198:201], v[14:17]
	v_mfma_f32_16x16x32_bf16 v[10:13], v[148:151], v[198:201], v[10:13]
	v_mfma_f32_16x16x32_bf16 v[54:57], v[152:155], v[168:171], v[54:57]
	v_mfma_f32_16x16x32_bf16 v[50:53], v[160:163], v[168:171], v[50:53]
	v_mfma_f32_16x16x32_bf16 v[38:41], v[152:155], v[176:179], v[38:41]
	v_mfma_f32_16x16x32_bf16 v[34:37], v[160:163], v[176:179], v[34:37]
	v_mfma_f32_16x16x32_bf16 v[22:25], v[152:155], v[186:189], v[22:25]
	v_mfma_f32_16x16x32_bf16 v[18:21], v[160:163], v[186:189], v[18:21]
	v_mfma_f32_16x16x32_bf16 v[6:9], v[152:155], v[194:197], v[6:9]
	v_mfma_f32_16x16x32_bf16 v[2:5], v[160:163], v[194:197], v[2:5]
	v_mfma_f32_16x16x32_bf16 v[54:57], v[156:159], v[172:175], v[54:57]
	v_mfma_f32_16x16x32_bf16 v[50:53], v[164:167], v[172:175], v[50:53]
	v_mfma_f32_16x16x32_bf16 v[38:41], v[156:159], v[182:185], v[38:41]
	v_mfma_f32_16x16x32_bf16 v[34:37], v[164:167], v[182:185], v[34:37]
	v_mfma_f32_16x16x32_bf16 v[22:25], v[156:159], v[190:193], v[22:25]
	v_mfma_f32_16x16x32_bf16 v[18:21], v[164:167], v[190:193], v[18:21]
	v_mfma_f32_16x16x32_bf16 v[6:9], v[156:159], v[198:201], v[6:9]
	v_mfma_f32_16x16x32_bf16 v[2:5], v[164:167], v[198:201], v[2:5]
	s_barrier
	s_setprio 0
	s_add_i32 s2, 0, 0x18000
	s_add_i32 s64, 0, 0x1c000
	v_add_u32_e32 v148, s2, v215
	v_add_u32_e32 v164, s64, v215
	ds_read_b128 v[136:139], v148
	ds_read_b128 v[140:143], v148 offset:1024
	ds_read_b128 v[144:147], v148 offset:2048
	ds_read_b128 v[148:151], v148 offset:3072
	ds_read_b128 v[152:155], v164
	ds_read_b128 v[156:159], v164 offset:1024
	ds_read_b128 v[160:163], v164 offset:2048
	ds_read_b128 v[164:167], v164 offset:3072
	s_add_u32 s28, s36, 0x40000
	s_addc_u32 s29, s37, 0
	s_mov_b32 m0, s46
	v_lshl_add_u64 v[210:211], s[28:29], 0, v[0:1]
	ds_read_b128 v[168:171], v181 offset:32768
	ds_read_b128 v[172:175], v181 offset:33792
	ds_read_b128 v[176:179], v181 offset:34816
	ds_read_b128 v[182:185], v181 offset:35840
	ds_read_b128 v[186:189], v181 offset:36864
	ds_read_b128 v[190:193], v181 offset:37888
	ds_read_b128 v[194:197], v181 offset:38912
	ds_read_b128 v[198:201], v181 offset:39936
	global_load_lds_dwordx4 v[210:211], off
	v_lshl_add_u64 v[210:211], s[28:29], 0, v[130:131]
	s_mov_b32 m0, s47
	s_nop 0
	global_load_lds_dwordx4 v[210:211], off
	s_waitcnt vmcnt(8)
	s_waitcnt lgkmcnt(0)
	s_setprio 1
	s_barrier
	v_mfma_f32_16x16x32_bf16 v[126:129], v[136:139], v[168:171], v[126:129]
	v_mfma_f32_16x16x32_bf16 v[122:125], v[144:147], v[168:171], v[122:125]
	v_mfma_f32_16x16x32_bf16 v[110:113], v[136:139], v[176:179], v[110:113]
	v_mfma_f32_16x16x32_bf16 v[106:109], v[144:147], v[176:179], v[106:109]
	v_mfma_f32_16x16x32_bf16 v[94:97], v[136:139], v[186:189], v[94:97]
	v_mfma_f32_16x16x32_bf16 v[90:93], v[144:147], v[186:189], v[90:93]
	v_mfma_f32_16x16x32_bf16 v[78:81], v[136:139], v[194:197], v[78:81]
	v_mfma_f32_16x16x32_bf16 v[74:77], v[144:147], v[194:197], v[74:77]
	v_mfma_f32_16x16x32_bf16 v[126:129], v[140:143], v[172:175], v[126:129]
	v_mfma_f32_16x16x32_bf16 v[122:125], v[148:151], v[172:175], v[122:125]
	v_mfma_f32_16x16x32_bf16 v[110:113], v[140:143], v[182:185], v[110:113]
	v_mfma_f32_16x16x32_bf16 v[106:109], v[148:151], v[182:185], v[106:109]
	v_mfma_f32_16x16x32_bf16 v[94:97], v[140:143], v[190:193], v[94:97]
	v_mfma_f32_16x16x32_bf16 v[90:93], v[148:151], v[190:193], v[90:93]
	v_mfma_f32_16x16x32_bf16 v[78:81], v[140:143], v[198:201], v[78:81]
	v_mfma_f32_16x16x32_bf16 v[74:77], v[148:151], v[198:201], v[74:77]
	v_mfma_f32_16x16x32_bf16 v[118:121], v[152:155], v[168:171], v[118:121]
	v_mfma_f32_16x16x32_bf16 v[114:117], v[160:163], v[168:171], v[114:117]
	v_mfma_f32_16x16x32_bf16 v[102:105], v[152:155], v[176:179], v[102:105]
	v_mfma_f32_16x16x32_bf16 v[98:101], v[160:163], v[176:179], v[98:101]
	v_mfma_f32_16x16x32_bf16 v[86:89], v[152:155], v[186:189], v[86:89]
	v_mfma_f32_16x16x32_bf16 v[82:85], v[160:163], v[186:189], v[82:85]
	v_mfma_f32_16x16x32_bf16 v[70:73], v[152:155], v[194:197], v[70:73]
	v_mfma_f32_16x16x32_bf16 v[66:69], v[160:163], v[194:197], v[66:69]
	v_mfma_f32_16x16x32_bf16 v[118:121], v[156:159], v[172:175], v[118:121]
	v_mfma_f32_16x16x32_bf16 v[114:117], v[164:167], v[172:175], v[114:117]
	v_mfma_f32_16x16x32_bf16 v[102:105], v[156:159], v[182:185], v[102:105]
	v_mfma_f32_16x16x32_bf16 v[98:101], v[164:167], v[182:185], v[98:101]
	v_mfma_f32_16x16x32_bf16 v[86:89], v[156:159], v[190:193], v[86:89]
	v_mfma_f32_16x16x32_bf16 v[82:85], v[164:167], v[190:193], v[82:85]
	v_mfma_f32_16x16x32_bf16 v[70:73], v[156:159], v[198:201], v[70:73]
	v_mfma_f32_16x16x32_bf16 v[66:69], v[164:167], v[198:201], v[66:69]
	s_barrier
; #define PG8_STAGE(bufoff, gbase, voff) do { _Pragma("unroll") for (int _i = 0; _i < 2; ++_i) \
;         __builtin_amdgcn_global_load_lds((const unsigned*)((const char*)(gbase) + (voff)[_i]), (PG8_LAS unsigned*)(lds + (bufoff) + ldsw + _i * 8192), 16, 0, 0); } while (0)
; #define PG8_LDA(dst, b, h) do { _Pragma("unroll") for (int m = 0; m < 4; ++m) _Pragma("unroll") for (int k = 0; k < 2; ++k) dst[m][k] = *(const PG8_LAS bf16x8*)(lds + PG8_SA(b, h) + aoff + m * 2048 + k * 1024); } while (0)
; #define PG8_MMA(ai, bj, At, Bt) do { __builtin_amdgcn_s_setprio(1); _Pragma("unroll") for (int m = 0; m < 4; ++m) _Pragma("unroll") for (int n = 0; n < 2; ++n) _Pragma("unroll") for (int k = 0; k < 2; ++k) \
;         acc[ai][bj][m][n] = __builtin_amdgcn_mfma_f32_16x16x32_bf16(Bt[n][k], At[m][k], acc[ai][bj][m][n], 0, 0, 0); __builtin_amdgcn_s_setprio(0); } while (0)
; #define PG8_WAIT_V(n) asm volatile("s_waitcnt vmcnt(" #n ")" ::: "memory")
; #define PG8_WAIT_L(n) asm volatile("s_waitcnt lgkmcnt(" #n ")" ::: "memory")
; #define PG8_BAR __builtin_amdgcn_s_barrier()
; #define PG8_SCHED __builtin_amdgcn_sched_barrier(0)
; template <class Epi, class Sched, bool ALIGN_EPI = false, bool SP2 = false, bool GATHER = false>
; __device__ __forceinline__ void gemm_phase(PG8_LAS unsigned char* lds, const Gemm g, const Sched& S, const Epi& E, const int2* gslot = nullptr, PG8_LAS unsigned char* gtab = nullptr) {
;     ...
;             PG8_LDA(At, 1, 1); PG8_STAGE(PG8_SB(1, 0), b3, voffB); PG8_STAGE(PG8_SB(1, 1), b3 + hstep, voffB); PG8_STAGE(PG8_SA(1, 0), a3, PG8_VA(vS, 0));
;             PG8_WAIT_V(8); PG8_WAIT_L(0); PG8_BAR; PG8_MMA(1, 0, At, B0); PG8_MMA(1, 1, At, B1); PG8_BAR; PG8_SCHED;
;     ...
;         if constexpr (ALIGN_EPI) { if (wr == 0) PG8_BAR; }
	s_setprio 0
	s_add_i32 s2, s2, s43
	v_lshl_add_u64 v[202:203], v[202:203], 0, s[54:55]
	s_mov_b32 m0, s2
	ds_read_b128 v[168:171], v181 offset:49152
	ds_read_b128 v[172:175], v181 offset:50176
	ds_read_b128 v[176:179], v181 offset:51200
	ds_read_b128 v[182:185], v181 offset:52224
	ds_read_b128 v[186:189], v181 offset:53248
	ds_read_b128 v[190:193], v181 offset:54272
	ds_read_b128 v[194:197], v181 offset:55296
	ds_read_b128 v[198:201], v181 offset:56320
	global_load_lds_dwordx4 v[202:203], off
	s_add_i32 m0, s2, 0x2000
	s_add_u32 s28, s34, 0x40080
	v_lshl_add_u64 v[202:203], v[204:205], 0, s[54:55]
	s_addc_u32 s29, s35, 0
	s_add_i32 s2, s64, s43
	global_load_lds_dwordx4 v[202:203], off
	v_lshl_add_u64 v[202:203], s[28:29], 0, v[0:1]
	s_mov_b32 m0, s2
	s_nop 0
	global_load_lds_dwordx4 v[202:203], off
	v_lshl_add_u64 v[202:203], s[28:29], 0, v[130:131]
	s_add_i32 m0, s2, 0x2000
	s_nop 0
	global_load_lds_dwordx4 v[202:203], off
	v_lshl_add_u64 v[202:203], v[206:207], 0, s[54:55]
	s_mov_b32 m0, s50
	s_nop 0
	global_load_lds_dwordx4 v[202:203], off
	v_lshl_add_u64 v[202:203], v[208:209], 0, s[54:55]
	s_mov_b32 m0, s51
	s_nop 0
	global_load_lds_dwordx4 v[202:203], off
	s_waitcnt vmcnt(8)
	s_waitcnt lgkmcnt(0)
	s_setprio 1
	s_barrier
	v_mfma_f32_16x16x32_bf16 v[62:65], v[136:139], v[168:171], v[62:65]
	v_mfma_f32_16x16x32_bf16 v[58:61], v[144:147], v[168:171], v[58:61]
	v_mfma_f32_16x16x32_bf16 v[46:49], v[136:139], v[176:179], v[46:49]
	v_mfma_f32_16x16x32_bf16 v[42:45], v[144:147], v[176:179], v[42:45]
	v_mfma_f32_16x16x32_bf16 v[30:33], v[136:139], v[186:189], v[30:33]
	v_mfma_f32_16x16x32_bf16 v[26:29], v[144:147], v[186:189], v[26:29]
	v_mfma_f32_16x16x32_bf16 v[14:17], v[136:139], v[194:197], v[14:17]
	v_mfma_f32_16x16x32_bf16 v[10:13], v[144:147], v[194:197], v[10:13]
	v_mfma_f32_16x16x32_bf16 v[62:65], v[140:143], v[172:175], v[62:65]
	v_mfma_f32_16x16x32_bf16 v[58:61], v[148:151], v[172:175], v[58:61]
	v_mfma_f32_16x16x32_bf16 v[46:49], v[140:143], v[182:185], v[46:49]
	v_mfma_f32_16x16x32_bf16 v[42:45], v[148:151], v[182:185], v[42:45]
	v_mfma_f32_16x16x32_bf16 v[30:33], v[140:143], v[190:193], v[30:33]
	v_mfma_f32_16x16x32_bf16 v[26:29], v[148:151], v[190:193], v[26:29]
	v_mfma_f32_16x16x32_bf16 v[14:17], v[140:143], v[198:201], v[14:17]
	v_mfma_f32_16x16x32_bf16 v[10:13], v[148:151], v[198:201], v[10:13]
	v_mfma_f32_16x16x32_bf16 v[54:57], v[152:155], v[168:171], v[54:57]
	v_mfma_f32_16x16x32_bf16 v[50:53], v[160:163], v[168:171], v[50:53]
	v_mfma_f32_16x16x32_bf16 v[38:41], v[152:155], v[176:179], v[38:41]
	v_mfma_f32_16x16x32_bf16 v[34:37], v[160:163], v[176:179], v[34:37]
	v_mfma_f32_16x16x32_bf16 v[22:25], v[152:155], v[186:189], v[22:25]
	v_mfma_f32_16x16x32_bf16 v[18:21], v[160:163], v[186:189], v[18:21]
	v_mfma_f32_16x16x32_bf16 v[6:9], v[152:155], v[194:197], v[6:9]
	v_mfma_f32_16x16x32_bf16 v[2:5], v[160:163], v[194:197], v[2:5]
	v_mfma_f32_16x16x32_bf16 v[54:57], v[156:159], v[172:175], v[54:57]
	v_mfma_f32_16x16x32_bf16 v[50:53], v[164:167], v[172:175], v[50:53]
	v_mfma_f32_16x16x32_bf16 v[38:41], v[156:159], v[182:185], v[38:41]
	v_mfma_f32_16x16x32_bf16 v[34:37], v[164:167], v[182:185], v[34:37]
	v_mfma_f32_16x16x32_bf16 v[22:25], v[156:159], v[190:193], v[22:25]
	v_mfma_f32_16x16x32_bf16 v[18:21], v[164:167], v[190:193], v[18:21]
	v_mfma_f32_16x16x32_bf16 v[6:9], v[156:159], v[198:201], v[6:9]
	v_mfma_f32_16x16x32_bf16 v[2:5], v[164:167], v[198:201], v[2:5]
	s_barrier
	s_setprio 0
	s_add_i32 s63, s63, 2
	s_add_u32 s61, s61, 0x100
	s_addc_u32 s62, s62, 0
	s_cmp_gt_u32 s63, 13
	s_mov_b64 s[28:29], s[30:31]
	s_cbranch_scc0 .LBB0_813
	s_and_b64 vcc, exec, s[18:19]
	s_cbranch_vccz .LBB0_816
	s_barrier

; #define PG8_GREAD(dst, u, par) do { _Pragma("unroll") for (int h_ = 0; h_ < 2; ++h_) _Pragma("unroll") for (int i_ = 0; i_ < 2; ++i_) { const int rl_ = 128 * h_ + grl[i_]; \
;         const int tk_ = *(const PG8_LAS int*)(gtab + (par) * 2048 + rl_ * 8); const unsigned tok_ = (rl_ < (u).rows) ? ((unsigned)tk_ >> 2) : 0u; dst[h_][i_] = tok_ * (unsigned)(K * 2) + gcb[i_]; } } while (0)
; #define PG8_STAGE(bufoff, gbase, voff) do { _Pragma("unroll") for (int _i = 0; _i < 2; ++_i) \
;         __builtin_amdgcn_global_load_lds((const unsigned*)((const char*)(gbase) + (voff)[_i]), (PG8_LAS unsigned*)(lds + (bufoff) + ldsw + _i * 8192), 16, 0, 0); } while (0)
; #define PG8_LDA(dst, b, h) do { _Pragma("unroll") for (int m = 0; m < 4; ++m) _Pragma("unroll") for (int k = 0; k < 2; ++k) dst[m][k] = *(const PG8_LAS bf16x8*)(lds + PG8_SA(b, h) + aoff + m * 2048 + k * 1024); } while (0)
; template <class Epi, class Sched, bool ALIGN_EPI = false, bool SP2 = false, bool GATHER = false>
; __device__ __forceinline__ void gemm_phase(PG8_LAS unsigned char* lds, const Gemm g, const Sched& S, const Epi& E, const int2* gslot = nullptr, PG8_LAS unsigned char* gtab = nullptr) {
;     ...
;             const char* a1 = cA + (size_t)(t + 1) * kstep;
;             const char* a2 = last ? nA : cA + (size_t)(t + 2) * kstep; const char* b2 = last ? nB : cB + (size_t)(t + 2) * kstep;
;             const char* a3 = a2 + kstep; const char* b3 = b2 + kstep;
;             if (last && has_next) S.a_ready(nxt);
;             if constexpr (GATHER) { if (last) { if (has_next) { PG8_GREAD(vN, nxt, (ui + 1) & 1); } else { _Pragma("unroll") for (int h_ = 0; h_ < 2; ++h_) _Pragma("unroll") for (int i_ = 0; i_ < 2; ++i_) vN[h_][i_] = vC[h_][i_]; } } }
;             unsigned vS[2][2];
; #pragma unroll
;             for (int h_ = 0; h_ < 2; ++h_)
; #pragma unroll
;                 for (int i_ = 0; i_ < 2; ++i_) vS[h_][i_] = (GATHER && last) ? vN[h_][i_] : vC[h_][i_];
;             if constexpr (SP2) {
;             PG8_LDB(B0, 0, 0); PG8_LDB(B1, 0, 1); PG8_SCHED; PG8_LDA(At, 0, 0); PG8_STAGE(PG8_SA(1, 1), a1 + PG8_AH(1), PG8_VA(vC, 1));
;             PG8_WAIT_V(8); PG8_WAIT_L(0); PG8_BAR; PG8_MMA(0, 0, At, B0); PG8_MMA(0, 1, At, B1); PG8_BAR; PG8_SCHED;
;             PG8_LDA(At, 0, 1); PG8_STAGE(PG8_SB(0, 0), b2, voffB); PG8_STAGE(PG8_SB(0, 1), b2 + hstep, voffB); PG8_STAGE(PG8_SA(0, 0), a2, PG8_VA(vS, 0));
.LBB0_1093:
	s_add_u32 s70, s18, s60
	s_addc_u32 s71, s19, s61
	s_add_u32 vcc_lo, s70, 0x34000100
	s_addc_u32 vcc_hi, s71, 0
	s_and_b64 s[70:71], s[72:73], exec
	s_cselect_b32 s71, s25, vcc_hi
	s_cselect_b32 s70, s24, vcc_lo
	s_add_u32 vcc_lo, s21, s60
	s_addc_u32 vcc_hi, s37, s61
	s_and_b64 s[72:73], s[72:73], exec
	s_cselect_b32 vcc_hi, s53, vcc_hi
	s_cselect_b32 vcc_lo, s52, vcc_lo
	s_add_i32 s72, 0, 0x10000
	v_add_u32_e32 v139, s72, v155
	s_add_i32 s2, 0, 0x14000
	ds_read_b128 v[140:143], v139
	ds_read_b128 v[162:165], v139 offset:1024
	ds_read_b128 v[180:183], v139 offset:2048
	ds_read_b128 v[188:191], v139 offset:3072
	v_add_u32_e32 v139, s2, v155
	ds_read_b128 v[192:195], v139
	ds_read_b128 v[196:199], v139 offset:1024
	ds_read_b128 v[200:203], v139 offset:2048
	ds_read_b128 v[204:207], v139 offset:3072
	v_lshl_add_u64 v[144:145], v[132:133], 0, s[60:61]
	s_add_i32 m0, s97, 0xc000
	ds_read_b128 v[208:211], v184
	ds_read_b128 v[212:215], v184 offset:1024
	ds_read_b128 v[216:219], v184 offset:2048
	ds_read_b128 v[220:223], v184 offset:3072
	ds_read_b128 v[224:227], v184 offset:4096
	ds_read_b128 v[230:233], v184 offset:5120
	ds_read_b128 v[236:239], v184 offset:6144
	ds_read_b128 v[240:243], v184 offset:7168
	global_load_lds_dwordx4 v[144:145], off
	v_lshl_add_u64 v[144:145], v[130:131], 0, s[60:61]
	s_add_i32 m0, s97, 0xe000
	s_nop 0
	global_load_lds_dwordx4 v[144:145], off
	s_waitcnt vmcnt(8)
	s_waitcnt lgkmcnt(0)
	s_setprio 1
	s_barrier
	v_mfma_f32_16x16x32_bf16 v[122:125], v[140:143], v[208:211], v[122:125]
	v_mfma_f32_16x16x32_bf16 v[114:117], v[180:183], v[208:211], v[114:117]
	v_mfma_f32_16x16x32_bf16 v[106:109], v[140:143], v[216:219], v[106:109]
	v_mfma_f32_16x16x32_bf16 v[98:101], v[180:183], v[216:219], v[98:101]
	v_mfma_f32_16x16x32_bf16 v[94:97], v[140:143], v[224:227], v[94:97]
	v_mfma_f32_16x16x32_bf16 v[90:93], v[180:183], v[224:227], v[90:93]
	v_mfma_f32_16x16x32_bf16 v[86:89], v[140:143], v[236:239], v[86:89]
	v_mfma_f32_16x16x32_bf16 v[82:85], v[180:183], v[236:239], v[82:85]
	v_mfma_f32_16x16x32_bf16 v[122:125], v[162:165], v[212:215], v[122:125]
	v_mfma_f32_16x16x32_bf16 v[114:117], v[188:191], v[212:215], v[114:117]
	v_mfma_f32_16x16x32_bf16 v[106:109], v[162:165], v[220:223], v[106:109]
	v_mfma_f32_16x16x32_bf16 v[98:101], v[188:191], v[220:223], v[98:101]
	v_mfma_f32_16x16x32_bf16 v[94:97], v[162:165], v[230:233], v[94:97]
	v_mfma_f32_16x16x32_bf16 v[90:93], v[188:191], v[230:233], v[90:93]
	v_mfma_f32_16x16x32_bf16 v[86:89], v[162:165], v[240:243], v[86:89]
	v_mfma_f32_16x16x32_bf16 v[82:85], v[188:191], v[240:243], v[82:85]
	v_mfma_f32_16x16x32_bf16 v[78:81], v[192:195], v[208:211], v[78:81]
	v_mfma_f32_16x16x32_bf16 v[74:77], v[200:203], v[208:211], v[74:77]
	v_mfma_f32_16x16x32_bf16 v[70:73], v[192:195], v[216:219], v[70:73]
	v_mfma_f32_16x16x32_bf16 v[66:69], v[200:203], v[216:219], v[66:69]
	v_mfma_f32_16x16x32_bf16 v[62:65], v[192:195], v[224:227], v[62:65]
	v_mfma_f32_16x16x32_bf16 v[58:61], v[200:203], v[224:227], v[58:61]
	v_mfma_f32_16x16x32_bf16 v[54:57], v[192:195], v[236:239], v[54:57]
	v_mfma_f32_16x16x32_bf16 v[50:53], v[200:203], v[236:239], v[50:53]
	v_mfma_f32_16x16x32_bf16 v[78:81], v[196:199], v[212:215], v[78:81]
	v_mfma_f32_16x16x32_bf16 v[74:77], v[204:207], v[212:215], v[74:77]
	v_mfma_f32_16x16x32_bf16 v[70:73], v[196:199], v[220:223], v[70:73]
	v_mfma_f32_16x16x32_bf16 v[66:69], v[204:207], v[220:223], v[66:69]
	v_mfma_f32_16x16x32_bf16 v[62:65], v[196:199], v[230:233], v[62:65]
	v_mfma_f32_16x16x32_bf16 v[58:61], v[204:207], v[230:233], v[58:61]
	v_mfma_f32_16x16x32_bf16 v[54:57], v[196:199], v[240:243], v[54:57]
	v_mfma_f32_16x16x32_bf16 v[50:53], v[204:207], v[240:243], v[50:53]
	s_barrier
	s_setprio 0
	s_add_i32 s72, s72, s47
	v_lshl_add_u64 v[166:167], vcc, 0, v[148:149]
	s_mov_b32 m0, s72
	ds_read_b128 v[208:211], v184 offset:16384
	ds_read_b128 v[212:215], v184 offset:17408
	ds_read_b128 v[216:219], v184 offset:18432
	ds_read_b128 v[220:223], v184 offset:19456
	ds_read_b128 v[224:227], v184 offset:20480
	ds_read_b128 v[230:233], v184 offset:21504
	ds_read_b128 v[236:239], v184 offset:22528
	ds_read_b128 v[240:243], v184 offset:23552
	global_load_lds_dwordx4 v[166:167], off
	s_add_i32 m0, s72, 0x2000
	s_add_u32 s72, vcc_lo, 0x40000
	v_lshl_add_u64 v[244:245], vcc, 0, v[150:151]
	s_addc_u32 s73, vcc_hi, 0
	s_add_i32 s2, s2, s47
	global_load_lds_dwordx4 v[244:245], off
	v_lshl_add_u64 v[144:145], s[72:73], 0, v[148:149]
	s_mov_b32 m0, s2
	v_mov_b32_e32 v139, v1
	global_load_lds_dwordx4 v[144:145], off
	v_lshl_add_u64 v[144:145], s[72:73], 0, v[150:151]
	s_add_i32 m0, s2, 0x2000
	v_lshl_add_u64 v[246:247], s[70:71], 0, v[0:1]
	global_load_lds_dwordx4 v[144:145], off
	s_mov_b32 m0, s97
	v_lshl_add_u64 v[248:249], s[70:71], 0, v[138:139]
	global_load_lds_dwordx4 v0, s[70:71]
	s_mov_b32 m0, s66
	s_nop 0
	global_load_lds_dwordx4 v138, s[70:71]
	s_waitcnt vmcnt(8)
	s_waitcnt lgkmcnt(0)
	s_setprio 1
	s_barrier
; #define PG8_STAGE(bufoff, gbase, voff) do { _Pragma("unroll") for (int _i = 0; _i < 2; ++_i) \
;         __builtin_amdgcn_global_load_lds((const unsigned*)((const char*)(gbase) + (voff)[_i]), (PG8_LAS unsigned*)(lds + (bufoff) + ldsw + _i * 8192), 16, 0, 0); } while (0)
; #define PG8_LDA(dst, b, h) do { _Pragma("unroll") for (int m = 0; m < 4; ++m) _Pragma("unroll") for (int k = 0; k < 2; ++k) dst[m][k] = *(const PG8_LAS bf16x8*)(lds + PG8_SA(b, h) + aoff + m * 2048 + k * 1024); } while (0)
; #define PG8_LDB(dst, b, h) do { _Pragma("unroll") for (int n = 0; n < 2; ++n) _Pragma("unroll") for (int k = 0; k < 2; ++k) dst[n][k] = *(const PG8_LAS bf16x8*)(lds + PG8_SB(b, h) + boff + n * 2048 + k * 1024); } while (0)
; #define PG8_MMA(ai, bj, At, Bt) do { __builtin_amdgcn_s_setprio(1); _Pragma("unroll") for (int m = 0; m < 4; ++m) _Pragma("unroll") for (int n = 0; n < 2; ++n) _Pragma("unroll") for (int k = 0; k < 2; ++k) \
;         acc[ai][bj][m][n] = __builtin_amdgcn_mfma_f32_16x16x32_bf16(Bt[n][k], At[m][k], acc[ai][bj][m][n], 0, 0, 0); __builtin_amdgcn_s_setprio(0); } while (0)
; #define PG8_WAIT_V(n) asm volatile("s_waitcnt vmcnt(" #n ")" ::: "memory")
; #define PG8_WAIT_L(n) asm volatile("s_waitcnt lgkmcnt(" #n ")" ::: "memory")
; #define PG8_BAR __builtin_amdgcn_s_barrier()
; #define PG8_SCHED __builtin_amdgcn_sched_barrier(0)
; template <class Epi, class Sched, bool ALIGN_EPI = false, bool SP2 = false, bool GATHER = false>
; __device__ __forceinline__ void gemm_phase(PG8_LAS unsigned char* lds, const Gemm g, const Sched& S, const Epi& E, const int2* gslot = nullptr, PG8_LAS unsigned char* gtab = nullptr) {
;     ...
;             PG8_LDA(At, 0, 1); PG8_STAGE(PG8_SB(0, 0), b2, voffB); PG8_STAGE(PG8_SB(0, 1), b2 + hstep, voffB); PG8_STAGE(PG8_SA(0, 0), a2, PG8_VA(vS, 0));
;             PG8_WAIT_V(8); PG8_WAIT_L(0); PG8_BAR; PG8_MMA(1, 0, At, B0); PG8_MMA(1, 1, At, B1); PG8_BAR; PG8_SCHED;
;             PG8_LDB(B0, 1, 0); PG8_LDB(B1, 1, 1); PG8_SCHED; PG8_LDA(At, 1, 0); PG8_STAGE(PG8_SA(0, 1), a2 + PG8_AH(1), PG8_VA(vS, 1));
;             PG8_WAIT_V(8); PG8_WAIT_L(0); PG8_BAR; PG8_MMA(0, 0, At, B0); PG8_MMA(0, 1, At, B1); PG8_BAR; PG8_SCHED;
	v_mfma_f32_16x16x32_bf16 v[46:49], v[140:143], v[208:211], v[46:49]
	v_mfma_f32_16x16x32_bf16 v[42:45], v[180:183], v[208:211], v[42:45]
	v_mfma_f32_16x16x32_bf16 v[38:41], v[140:143], v[216:219], v[38:41]
	v_mfma_f32_16x16x32_bf16 v[34:37], v[180:183], v[216:219], v[34:37]
	v_mfma_f32_16x16x32_bf16 v[30:33], v[140:143], v[224:227], v[30:33]
	v_mfma_f32_16x16x32_bf16 v[26:29], v[180:183], v[224:227], v[26:29]
	v_mfma_f32_16x16x32_bf16 v[6:9], v[140:143], v[236:239], v[6:9]
	v_mfma_f32_16x16x32_bf16 v[2:5], v[180:183], v[236:239], v[2:5]
	v_mfma_f32_16x16x32_bf16 v[46:49], v[162:165], v[212:215], v[46:49]
	v_mfma_f32_16x16x32_bf16 v[42:45], v[188:191], v[212:215], v[42:45]
	v_mfma_f32_16x16x32_bf16 v[38:41], v[162:165], v[220:223], v[38:41]
	v_mfma_f32_16x16x32_bf16 v[34:37], v[188:191], v[220:223], v[34:37]
	v_mfma_f32_16x16x32_bf16 v[30:33], v[162:165], v[230:233], v[30:33]
	v_mfma_f32_16x16x32_bf16 v[26:29], v[188:191], v[230:233], v[26:29]
	v_mfma_f32_16x16x32_bf16 v[6:9], v[162:165], v[240:243], v[6:9]
	v_mfma_f32_16x16x32_bf16 v[2:5], v[188:191], v[240:243], v[2:5]
	v_mfma_f32_16x16x32_bf16 v[22:25], v[192:195], v[208:211], v[22:25]
	v_mfma_f32_16x16x32_bf16 v[18:21], v[200:203], v[208:211], v[18:21]
	v_mfma_f32_16x16x32_bf16 v[14:17], v[192:195], v[216:219], v[14:17]
	v_mfma_f32_16x16x32_bf16 v[10:13], v[200:203], v[216:219], v[10:13]
	v_mfma_f32_16x16x32_bf16 v[102:105], v[192:195], v[224:227], v[102:105]
	v_mfma_f32_16x16x32_bf16 v[110:113], v[200:203], v[224:227], v[110:113]
	v_mfma_f32_16x16x32_bf16 v[118:121], v[192:195], v[236:239], v[118:121]
	v_mfma_f32_16x16x32_bf16 v[126:129], v[200:203], v[236:239], v[126:129]
	v_mfma_f32_16x16x32_bf16 v[22:25], v[196:199], v[212:215], v[22:25]
	v_mfma_f32_16x16x32_bf16 v[18:21], v[204:207], v[212:215], v[18:21]
	v_mfma_f32_16x16x32_bf16 v[14:17], v[196:199], v[220:223], v[14:17]
	v_mfma_f32_16x16x32_bf16 v[10:13], v[204:207], v[220:223], v[10:13]
	v_mfma_f32_16x16x32_bf16 v[102:105], v[196:199], v[230:233], v[102:105]
	v_mfma_f32_16x16x32_bf16 v[110:113], v[204:207], v[230:233], v[110:113]
	v_mfma_f32_16x16x32_bf16 v[118:121], v[196:199], v[240:243], v[118:121]
	v_mfma_f32_16x16x32_bf16 v[126:129], v[204:207], v[240:243], v[126:129]
	s_barrier
	s_setprio 0
	s_add_i32 s2, 0, 0x18000
	v_add_u32_e32 v0, s2, v155
	s_add_i32 s72, 0, 0x1c000
	ds_read_b128 v[138:141], v0
	ds_read_b128 v[142:145], v0 offset:1024
	ds_read_b128 v[162:165], v0 offset:2048
	ds_read_b128 v[180:183], v0 offset:3072
	v_add_u32_e32 v0, s72, v155
	ds_read_b128 v[188:191], v0
	ds_read_b128 v[192:195], v0 offset:1024
	ds_read_b128 v[196:199], v0 offset:2048
	ds_read_b128 v[200:203], v0 offset:3072
	s_mov_b32 m0, s67
	v_lshl_add_u64 v[136:137], s[70:71], 0, v[136:137]
	ds_read_b128 v[204:207], v184 offset:32768
	ds_read_b128 v[208:211], v184 offset:33792
	ds_read_b128 v[212:215], v184 offset:34816
	ds_read_b128 v[216:219], v184 offset:35840
	ds_read_b128 v[220:223], v184 offset:36864
	ds_read_b128 v[224:227], v184 offset:37888
	ds_read_b128 v[230:233], v184 offset:38912
	ds_read_b128 v[236:239], v184 offset:39936
	global_load_lds_dwordx4 v[136:137], off
	v_lshl_add_u64 v[134:135], s[70:71], 0, v[134:135]
	s_mov_b32 m0, s56
	s_nop 0
	global_load_lds_dwordx4 v[134:135], off
	s_waitcnt vmcnt(8)
	s_waitcnt lgkmcnt(0)
	s_setprio 1
	s_barrier
	v_mfma_f32_16x16x32_bf16 v[122:125], v[138:141], v[204:207], v[122:125]
	v_mfma_f32_16x16x32_bf16 v[114:117], v[162:165], v[204:207], v[114:117]
	v_mfma_f32_16x16x32_bf16 v[106:109], v[138:141], v[212:215], v[106:109]
	v_mfma_f32_16x16x32_bf16 v[98:101], v[162:165], v[212:215], v[98:101]
	v_mfma_f32_16x16x32_bf16 v[94:97], v[138:141], v[220:223], v[94:97]
	v_mfma_f32_16x16x32_bf16 v[90:93], v[162:165], v[220:223], v[90:93]
	v_mfma_f32_16x16x32_bf16 v[86:89], v[138:141], v[230:233], v[86:89]
	v_mfma_f32_16x16x32_bf16 v[82:85], v[162:165], v[230:233], v[82:85]
	v_mfma_f32_16x16x32_bf16 v[122:125], v[142:145], v[208:211], v[122:125]
	v_mfma_f32_16x16x32_bf16 v[114:117], v[180:183], v[208:211], v[114:117]
	v_mfma_f32_16x16x32_bf16 v[106:109], v[142:145], v[216:219], v[106:109]
	v_mfma_f32_16x16x32_bf16 v[98:101], v[180:183], v[216:219], v[98:101]
	v_mfma_f32_16x16x32_bf16 v[94:97], v[142:145], v[224:227], v[94:97]
	v_mfma_f32_16x16x32_bf16 v[90:93], v[180:183], v[224:227], v[90:93]
	v_mfma_f32_16x16x32_bf16 v[86:89], v[142:145], v[236:239], v[86:89]
	v_mfma_f32_16x16x32_bf16 v[82:85], v[180:183], v[236:239], v[82:85]
	v_mfma_f32_16x16x32_bf16 v[78:81], v[188:191], v[204:207], v[78:81]
	v_mfma_f32_16x16x32_bf16 v[74:77], v[196:199], v[204:207], v[74:77]
	v_mfma_f32_16x16x32_bf16 v[70:73], v[188:191], v[212:215], v[70:73]
	v_mfma_f32_16x16x32_bf16 v[66:69], v[196:199], v[212:215], v[66:69]
	v_mfma_f32_16x16x32_bf16 v[62:65], v[188:191], v[220:223], v[62:65]
	v_mfma_f32_16x16x32_bf16 v[58:61], v[196:199], v[220:223], v[58:61]
	v_mfma_f32_16x16x32_bf16 v[54:57], v[188:191], v[230:233], v[54:57]
	v_mfma_f32_16x16x32_bf16 v[50:53], v[196:199], v[230:233], v[50:53]
	v_mfma_f32_16x16x32_bf16 v[78:81], v[192:195], v[208:211], v[78:81]
	v_mfma_f32_16x16x32_bf16 v[74:77], v[200:203], v[208:211], v[74:77]
	v_mfma_f32_16x16x32_bf16 v[70:73], v[192:195], v[216:219], v[70:73]
	v_mfma_f32_16x16x32_bf16 v[66:69], v[200:203], v[216:219], v[66:69]
	v_mfma_f32_16x16x32_bf16 v[62:65], v[192:195], v[224:227], v[62:65]
	v_mfma_f32_16x16x32_bf16 v[58:61], v[200:203], v[224:227], v[58:61]
	v_mfma_f32_16x16x32_bf16 v[54:57], v[192:195], v[236:239], v[54:57]
	v_mfma_f32_16x16x32_bf16 v[50:53], v[200:203], v[236:239], v[50:53]
	s_barrier
; #define PG8_STAGE(bufoff, gbase, voff) do { _Pragma("unroll") for (int _i = 0; _i < 2; ++_i) \
;         __builtin_amdgcn_global_load_lds((const unsigned*)((const char*)(gbase) + (voff)[_i]), (PG8_LAS unsigned*)(lds + (bufoff) + ldsw + _i * 8192), 16, 0, 0); } while (0)
; #define PG8_LDA(dst, b, h) do { _Pragma("unroll") for (int m = 0; m < 4; ++m) _Pragma("unroll") for (int k = 0; k < 2; ++k) dst[m][k] = *(const PG8_LAS bf16x8*)(lds + PG8_SA(b, h) + aoff + m * 2048 + k * 1024); } while (0)
; #define PG8_MMA(ai, bj, At, Bt) do { __builtin_amdgcn_s_setprio(1); _Pragma("unroll") for (int m = 0; m < 4; ++m) _Pragma("unroll") for (int n = 0; n < 2; ++n) _Pragma("unroll") for (int k = 0; k < 2; ++k) \
;         acc[ai][bj][m][n] = __builtin_amdgcn_mfma_f32_16x16x32_bf16(Bt[n][k], At[m][k], acc[ai][bj][m][n], 0, 0, 0); __builtin_amdgcn_s_setprio(0); } while (0)
; #define PG8_WAIT_V(n) asm volatile("s_waitcnt vmcnt(" #n ")" ::: "memory")
; #define PG8_WAIT_L(n) asm volatile("s_waitcnt lgkmcnt(" #n ")" ::: "memory")
; #define PG8_BAR __builtin_amdgcn_s_barrier()
; #define PG8_SCHED __builtin_amdgcn_sched_barrier(0)
; template <class Epi, class Sched, bool ALIGN_EPI = false, bool SP2 = false, bool GATHER = false>
; __device__ __forceinline__ void gemm_phase(PG8_LAS unsigned char* lds, const Gemm g, const Sched& S, const Epi& E, const int2* gslot = nullptr, PG8_LAS unsigned char* gtab = nullptr) {
;     ...
;             PG8_LDA(At, 1, 1); PG8_STAGE(PG8_SB(1, 0), b3, voffB); PG8_STAGE(PG8_SB(1, 1), b3 + hstep, voffB); PG8_STAGE(PG8_SA(1, 0), a3, PG8_VA(vS, 0));
;             PG8_WAIT_V(8); PG8_WAIT_L(0); PG8_BAR; PG8_MMA(1, 0, At, B0); PG8_MMA(1, 1, At, B1); PG8_BAR; PG8_SCHED;
	s_setprio 0
	s_add_i32 s2, s2, s47
	v_lshl_add_u64 v[166:167], v[166:167], 0, s[54:55]
	s_mov_b32 m0, s2
	ds_read_b128 v[134:137], v184 offset:49152
	ds_read_b128 v[204:207], v184 offset:50176
	ds_read_b128 v[208:211], v184 offset:51200
	ds_read_b128 v[212:215], v184 offset:52224
	ds_read_b128 v[216:219], v184 offset:53248
	ds_read_b128 v[220:223], v184 offset:54272
	ds_read_b128 v[224:227], v184 offset:55296
	ds_read_b128 v[230:233], v184 offset:56320
	global_load_lds_dwordx4 v[166:167], off
	s_add_i32 m0, s2, 0x2000
	s_add_u32 s70, vcc_lo, 0x40080
	v_lshl_add_u64 v[166:167], v[244:245], 0, s[54:55]
	s_addc_u32 s71, vcc_hi, 0
	s_add_i32 s2, s72, s47
	global_load_lds_dwordx4 v[166:167], off
	v_lshl_add_u64 v[166:167], s[70:71], 0, v[148:149]
	s_mov_b32 m0, s2
	s_nop 0
	global_load_lds_dwordx4 v[166:167], off
	v_lshl_add_u64 v[166:167], s[70:71], 0, v[150:151]
	s_add_i32 m0, s2, 0x2000
	s_nop 0
	global_load_lds_dwordx4 v[166:167], off
	v_lshl_add_u64 v[166:167], v[246:247], 0, s[54:55]
	s_mov_b32 m0, s0
	s_nop 0
	global_load_lds_dwordx4 v[166:167], off
	v_lshl_add_u64 v[166:167], v[248:249], 0, s[54:55]
	s_mov_b32 m0, s43
	s_nop 0
	global_load_lds_dwordx4 v[166:167], off
	s_waitcnt vmcnt(8)
	s_waitcnt lgkmcnt(0)
	s_setprio 1
	s_barrier
	v_mfma_f32_16x16x32_bf16 v[46:49], v[138:141], v[134:137], v[46:49]
	v_mfma_f32_16x16x32_bf16 v[42:45], v[162:165], v[134:137], v[42:45]
	v_mfma_f32_16x16x32_bf16 v[38:41], v[138:141], v[208:211], v[38:41]
	v_mfma_f32_16x16x32_bf16 v[34:37], v[162:165], v[208:211], v[34:37]
	v_mfma_f32_16x16x32_bf16 v[30:33], v[138:141], v[216:219], v[30:33]
	v_mfma_f32_16x16x32_bf16 v[26:29], v[162:165], v[216:219], v[26:29]
	v_mfma_f32_16x16x32_bf16 v[6:9], v[138:141], v[224:227], v[6:9]
	v_mfma_f32_16x16x32_bf16 v[2:5], v[162:165], v[224:227], v[2:5]
	v_mfma_f32_16x16x32_bf16 v[46:49], v[142:145], v[204:207], v[46:49]
	v_mfma_f32_16x16x32_bf16 v[42:45], v[180:183], v[204:207], v[42:45]
	v_mfma_f32_16x16x32_bf16 v[38:41], v[142:145], v[212:215], v[38:41]
	v_mfma_f32_16x16x32_bf16 v[34:37], v[180:183], v[212:215], v[34:37]
	v_mfma_f32_16x16x32_bf16 v[30:33], v[142:145], v[220:223], v[30:33]
	v_mfma_f32_16x16x32_bf16 v[26:29], v[180:183], v[220:223], v[26:29]
	v_mfma_f32_16x16x32_bf16 v[6:9], v[142:145], v[230:233], v[6:9]
	v_mfma_f32_16x16x32_bf16 v[2:5], v[180:183], v[230:233], v[2:5]
	v_mfma_f32_16x16x32_bf16 v[22:25], v[188:191], v[134:137], v[22:25]
	v_mfma_f32_16x16x32_bf16 v[18:21], v[196:199], v[134:137], v[18:21]
	v_mfma_f32_16x16x32_bf16 v[14:17], v[188:191], v[208:211], v[14:17]
	v_mfma_f32_16x16x32_bf16 v[10:13], v[196:199], v[208:211], v[10:13]
	v_mfma_f32_16x16x32_bf16 v[102:105], v[188:191], v[216:219], v[102:105]
	v_mfma_f32_16x16x32_bf16 v[110:113], v[196:199], v[216:219], v[110:113]
	v_mfma_f32_16x16x32_bf16 v[118:121], v[188:191], v[224:227], v[118:121]
	v_mfma_f32_16x16x32_bf16 v[126:129], v[196:199], v[224:227], v[126:129]
	v_mfma_f32_16x16x32_bf16 v[22:25], v[192:195], v[204:207], v[22:25]
	v_mfma_f32_16x16x32_bf16 v[18:21], v[200:203], v[204:207], v[18:21]
	v_mfma_f32_16x16x32_bf16 v[14:17], v[192:195], v[212:215], v[14:17]
	v_mfma_f32_16x16x32_bf16 v[10:13], v[200:203], v[212:215], v[10:13]
	v_mfma_f32_16x16x32_bf16 v[102:105], v[192:195], v[220:223], v[102:105]
	v_mfma_f32_16x16x32_bf16 v[110:113], v[200:203], v[220:223], v[110:113]
	v_mfma_f32_16x16x32_bf16 v[118:121], v[192:195], v[230:233], v[118:121]
	v_mfma_f32_16x16x32_bf16 v[126:129], v[200:203], v[230:233], v[126:129]
	s_barrier
	s_setprio 0
	s_add_i32 s69, s69, 2
	s_add_u32 s60, s60, 0x100
	s_addc_u32 s61, s61, 0
	s_cmp_gt_u32 s69, 13
	s_cbranch_scc1 .LBB0_1097

; #define PG8_GREAD(dst, u, par) do { _Pragma("unroll") for (int h_ = 0; h_ < 2; ++h_) _Pragma("unroll") for (int i_ = 0; i_ < 2; ++i_) { const int rl_ = 128 * h_ + grl[i_]; \
;         const int tk_ = *(const PG8_LAS int*)(gtab + (par) * 2048 + rl_ * 8); const unsigned tok_ = (rl_ < (u).rows) ? ((unsigned)tk_ >> 2) : 0u; dst[h_][i_] = tok_ * (unsigned)(K * 2) + gcb[i_]; } } while (0)
; #define PG8_STAGE(bufoff, gbase, voff) do { _Pragma("unroll") for (int _i = 0; _i < 2; ++_i) \
;         __builtin_amdgcn_global_load_lds((const unsigned*)((const char*)(gbase) + (voff)[_i]), (PG8_LAS unsigned*)(lds + (bufoff) + ldsw + _i * 8192), 16, 0, 0); } while (0)
; #define PG8_LDA(dst, b, h) do { _Pragma("unroll") for (int m = 0; m < 4; ++m) _Pragma("unroll") for (int k = 0; k < 2; ++k) dst[m][k] = *(const PG8_LAS bf16x8*)(lds + PG8_SA(b, h) + aoff + m * 2048 + k * 1024); } while (0)
; template <class Epi, class Sched, bool ALIGN_EPI = false, bool SP2 = false, bool GATHER = false>
; __device__ __forceinline__ void gemm_phase(PG8_LAS unsigned char* lds, const Gemm g, const Sched& S, const Epi& E, const int2* gslot = nullptr, PG8_LAS unsigned char* gtab = nullptr) {
;     ...
;             const char* a1 = cA + (size_t)(t + 1) * kstep;
;             const char* a2 = last ? nA : cA + (size_t)(t + 2) * kstep; const char* b2 = last ? nB : cB + (size_t)(t + 2) * kstep;
;             const char* a3 = a2 + kstep; const char* b3 = b2 + kstep;
;             if (last && has_next) S.a_ready(nxt);
;             if constexpr (GATHER) { if (last) { if (has_next) { PG8_GREAD(vN, nxt, (ui + 1) & 1); } else { _Pragma("unroll") for (int h_ = 0; h_ < 2; ++h_) _Pragma("unroll") for (int i_ = 0; i_ < 2; ++i_) vN[h_][i_] = vC[h_][i_]; } } }
;             unsigned vS[2][2];
; #pragma unroll
;             for (int h_ = 0; h_ < 2; ++h_)
; #pragma unroll
;                 for (int i_ = 0; i_ < 2; ++i_) vS[h_][i_] = (GATHER && last) ? vN[h_][i_] : vC[h_][i_];
;             if constexpr (SP2) {
;             PG8_LDB(B0, 0, 0); PG8_LDB(B1, 0, 1); PG8_SCHED; PG8_LDA(At, 0, 0); PG8_STAGE(PG8_SA(1, 1), a1 + PG8_AH(1), PG8_VA(vC, 1));
;             PG8_WAIT_V(8); PG8_WAIT_L(0); PG8_BAR; PG8_MMA(0, 0, At, B0); PG8_MMA(0, 1, At, B1); PG8_BAR; PG8_SCHED;
;             PG8_LDA(At, 0, 1); PG8_STAGE(PG8_SB(0, 0), b2, voffB); PG8_STAGE(PG8_SB(0, 1), b2 + hstep, voffB); PG8_STAGE(PG8_SA(0, 0), a2, PG8_VA(vS, 0));
.LBB0_1174:
	s_add_u32 s2, s12, 0xfffc0080
	s_addc_u32 s10, s13, -1
	s_cmp_eq_u32 s67, 12
	s_cselect_b32 s15, s7, s10
	s_cselect_b32 s14, s9, s2
	s_cselect_b32 s11, s18, s29
	s_cselect_b32 s10, s19, s27
	s_add_i32 s2, 0, 0x10000
	s_add_i32 s70, 0, 0x14000
	v_add_u32_e32 v78, s2, v168
	v_add_u32_e32 v164, s70, v168
	ds_read_b128 v[66:69], v78
	ds_read_b128 v[70:73], v78 offset:1024
	ds_read_b128 v[74:77], v78 offset:2048
	ds_read_b128 v[78:81], v78 offset:3072
	ds_read_b128 v[156:159], v164
	ds_read_b128 v[160:163], v164 offset:1024
	ds_read_b128 v[172:175], v164 offset:2048
	ds_read_b128 v[176:179], v164 offset:3072
	v_lshl_add_u64 v[164:165], s[12:13], 0, v[152:153]
	s_add_i32 m0, s47, 0xc000
	ds_read_b128 v[180:183], v170
	ds_read_b128 v[184:187], v170 offset:1024
	ds_read_b128 v[188:191], v170 offset:2048
	ds_read_b128 v[192:195], v170 offset:3072
	ds_read_b128 v[196:199], v170 offset:4096
	ds_read_b128 v[200:203], v170 offset:5120
	ds_read_b128 v[204:207], v170 offset:6144
	ds_read_b128 v[208:211], v170 offset:7168
	global_load_lds_dwordx4 v[164:165], off
	v_lshl_add_u64 v[164:165], s[12:13], 0, v[154:155]
	s_add_i32 m0, s47, 0xe000
	s_nop 0
	global_load_lds_dwordx4 v[164:165], off
	s_waitcnt vmcnt(8)
	s_waitcnt lgkmcnt(0)
	s_setprio 1
	s_barrier
	v_mfma_f32_16x16x32_bf16 v[142:145], v[66:69], v[180:183], v[142:145]
	v_mfma_f32_16x16x32_bf16 v[138:141], v[74:77], v[180:183], v[138:141]
	v_mfma_f32_16x16x32_bf16 v[126:129], v[66:69], v[188:191], v[126:129]
	v_mfma_f32_16x16x32_bf16 v[122:125], v[74:77], v[188:191], v[122:125]
	v_mfma_f32_16x16x32_bf16 v[110:113], v[66:69], v[196:199], v[110:113]
	v_mfma_f32_16x16x32_bf16 v[106:109], v[74:77], v[196:199], v[106:109]
	v_mfma_f32_16x16x32_bf16 v[94:97], v[66:69], v[204:207], v[94:97]
	v_mfma_f32_16x16x32_bf16 v[90:93], v[74:77], v[204:207], v[90:93]
	v_mfma_f32_16x16x32_bf16 v[142:145], v[70:73], v[184:187], v[142:145]
	v_mfma_f32_16x16x32_bf16 v[138:141], v[78:81], v[184:187], v[138:141]
	v_mfma_f32_16x16x32_bf16 v[126:129], v[70:73], v[192:195], v[126:129]
	v_mfma_f32_16x16x32_bf16 v[122:125], v[78:81], v[192:195], v[122:125]
	v_mfma_f32_16x16x32_bf16 v[110:113], v[70:73], v[200:203], v[110:113]
	v_mfma_f32_16x16x32_bf16 v[106:109], v[78:81], v[200:203], v[106:109]
	v_mfma_f32_16x16x32_bf16 v[94:97], v[70:73], v[208:211], v[94:97]
	v_mfma_f32_16x16x32_bf16 v[90:93], v[78:81], v[208:211], v[90:93]
	v_mfma_f32_16x16x32_bf16 v[134:137], v[156:159], v[180:183], v[134:137]
	v_mfma_f32_16x16x32_bf16 v[130:133], v[172:175], v[180:183], v[130:133]
	v_mfma_f32_16x16x32_bf16 v[118:121], v[156:159], v[188:191], v[118:121]
	v_mfma_f32_16x16x32_bf16 v[114:117], v[172:175], v[188:191], v[114:117]
	v_mfma_f32_16x16x32_bf16 v[102:105], v[156:159], v[196:199], v[102:105]
	v_mfma_f32_16x16x32_bf16 v[98:101], v[172:175], v[196:199], v[98:101]
	v_mfma_f32_16x16x32_bf16 v[86:89], v[156:159], v[204:207], v[86:89]
	v_mfma_f32_16x16x32_bf16 v[82:85], v[172:175], v[204:207], v[82:85]
	v_mfma_f32_16x16x32_bf16 v[134:137], v[160:163], v[184:187], v[134:137]
	v_mfma_f32_16x16x32_bf16 v[130:133], v[176:179], v[184:187], v[130:133]
	v_mfma_f32_16x16x32_bf16 v[118:121], v[160:163], v[192:195], v[118:121]
	v_mfma_f32_16x16x32_bf16 v[114:117], v[176:179], v[192:195], v[114:117]
	v_mfma_f32_16x16x32_bf16 v[102:105], v[160:163], v[200:203], v[102:105]
	v_mfma_f32_16x16x32_bf16 v[98:101], v[176:179], v[200:203], v[98:101]
	v_mfma_f32_16x16x32_bf16 v[86:89], v[160:163], v[208:211], v[86:89]
	v_mfma_f32_16x16x32_bf16 v[82:85], v[176:179], v[208:211], v[82:85]
	s_barrier
	s_setprio 0
	s_add_i32 s2, s2, s45
	v_lshl_add_u64 v[164:165], s[10:11], 0, v[0:1]
	s_mov_b32 m0, s2
	ds_read_b128 v[180:183], v170 offset:16384
	ds_read_b128 v[184:187], v170 offset:17408
	ds_read_b128 v[188:191], v170 offset:18432
	ds_read_b128 v[192:195], v170 offset:19456
	ds_read_b128 v[196:199], v170 offset:20480
	ds_read_b128 v[200:203], v170 offset:21504
	ds_read_b128 v[204:207], v170 offset:22528
	ds_read_b128 v[208:211], v170 offset:23552
	global_load_lds_dwordx4 v[164:165], off
	s_add_i32 m0, s2, 0x2000
	s_add_u32 s68, s10, 0x40000
	v_lshl_add_u64 v[212:213], s[10:11], 0, v[146:147]
	s_addc_u32 s69, s11, 0
	s_add_i32 s2, s70, s45
	global_load_lds_dwordx4 v[212:213], off
	v_lshl_add_u64 v[214:215], s[68:69], 0, v[0:1]
	s_mov_b32 m0, s2
	v_lshl_add_u64 v[216:217], s[14:15], 0, v[148:149]
	global_load_lds_dwordx4 v[214:215], off
	v_lshl_add_u64 v[214:215], s[68:69], 0, v[146:147]
	s_add_i32 m0, s2, 0x2000
	s_nop 0
	global_load_lds_dwordx4 v[214:215], off
	v_lshl_add_u64 v[214:215], s[14:15], 0, v[150:151]
	s_mov_b32 m0, s47
	s_nop 0
	global_load_lds_dwordx4 v[214:215], off
	s_mov_b32 m0, s50
	s_nop 0
	global_load_lds_dwordx4 v[216:217], off
	s_waitcnt vmcnt(8)
	s_waitcnt lgkmcnt(0)
	s_setprio 1
	s_barrier
; #define PG8_STAGE(bufoff, gbase, voff) do { _Pragma("unroll") for (int _i = 0; _i < 2; ++_i) \
;         __builtin_amdgcn_global_load_lds((const unsigned*)((const char*)(gbase) + (voff)[_i]), (PG8_LAS unsigned*)(lds + (bufoff) + ldsw + _i * 8192), 16, 0, 0); } while (0)
; #define PG8_LDA(dst, b, h) do { _Pragma("unroll") for (int m = 0; m < 4; ++m) _Pragma("unroll") for (int k = 0; k < 2; ++k) dst[m][k] = *(const PG8_LAS bf16x8*)(lds + PG8_SA(b, h) + aoff + m * 2048 + k * 1024); } while (0)
; #define PG8_LDB(dst, b, h) do { _Pragma("unroll") for (int n = 0; n < 2; ++n) _Pragma("unroll") for (int k = 0; k < 2; ++k) dst[n][k] = *(const PG8_LAS bf16x8*)(lds + PG8_SB(b, h) + boff + n * 2048 + k * 1024); } while (0)
; #define PG8_MMA(ai, bj, At, Bt) do { __builtin_amdgcn_s_setprio(1); _Pragma("unroll") for (int m = 0; m < 4; ++m) _Pragma("unroll") for (int n = 0; n < 2; ++n) _Pragma("unroll") for (int k = 0; k < 2; ++k) \
;         acc[ai][bj][m][n] = __builtin_amdgcn_mfma_f32_16x16x32_bf16(Bt[n][k], At[m][k], acc[ai][bj][m][n], 0, 0, 0); __builtin_amdgcn_s_setprio(0); } while (0)
; #define PG8_WAIT_V(n) asm volatile("s_waitcnt vmcnt(" #n ")" ::: "memory")
; #define PG8_WAIT_L(n) asm volatile("s_waitcnt lgkmcnt(" #n ")" ::: "memory")
; #define PG8_BAR __builtin_amdgcn_s_barrier()
; #define PG8_SCHED __builtin_amdgcn_sched_barrier(0)
; template <class Epi, class Sched, bool ALIGN_EPI = false, bool SP2 = false, bool GATHER = false>
; __device__ __forceinline__ void gemm_phase(PG8_LAS unsigned char* lds, const Gemm g, const Sched& S, const Epi& E, const int2* gslot = nullptr, PG8_LAS unsigned char* gtab = nullptr) {
;     ...
;             PG8_LDA(At, 0, 1); PG8_STAGE(PG8_SB(0, 0), b2, voffB); PG8_STAGE(PG8_SB(0, 1), b2 + hstep, voffB); PG8_STAGE(PG8_SA(0, 0), a2, PG8_VA(vS, 0));
;             PG8_WAIT_V(8); PG8_WAIT_L(0); PG8_BAR; PG8_MMA(1, 0, At, B0); PG8_MMA(1, 1, At, B1); PG8_BAR; PG8_SCHED;
;             PG8_LDB(B0, 1, 0); PG8_LDB(B1, 1, 1); PG8_SCHED; PG8_LDA(At, 1, 0); PG8_STAGE(PG8_SA(0, 1), a2 + PG8_AH(1), PG8_VA(vS, 1));
;             PG8_WAIT_V(8); PG8_WAIT_L(0); PG8_BAR; PG8_MMA(0, 0, At, B0); PG8_MMA(0, 1, At, B1); PG8_BAR; PG8_SCHED;
	v_mfma_f32_16x16x32_bf16 v[62:65], v[66:69], v[180:183], v[62:65]
	v_mfma_f32_16x16x32_bf16 v[58:61], v[74:77], v[180:183], v[58:61]
	v_mfma_f32_16x16x32_bf16 v[46:49], v[66:69], v[188:191], v[46:49]
	v_mfma_f32_16x16x32_bf16 v[42:45], v[74:77], v[188:191], v[42:45]
	v_mfma_f32_16x16x32_bf16 v[30:33], v[66:69], v[196:199], v[30:33]
	v_mfma_f32_16x16x32_bf16 v[26:29], v[74:77], v[196:199], v[26:29]
	v_mfma_f32_16x16x32_bf16 v[14:17], v[66:69], v[204:207], v[14:17]
	v_mfma_f32_16x16x32_bf16 v[10:13], v[74:77], v[204:207], v[10:13]
	v_mfma_f32_16x16x32_bf16 v[62:65], v[70:73], v[184:187], v[62:65]
	v_mfma_f32_16x16x32_bf16 v[58:61], v[78:81], v[184:187], v[58:61]
	v_mfma_f32_16x16x32_bf16 v[46:49], v[70:73], v[192:195], v[46:49]
	v_mfma_f32_16x16x32_bf16 v[42:45], v[78:81], v[192:195], v[42:45]
	v_mfma_f32_16x16x32_bf16 v[30:33], v[70:73], v[200:203], v[30:33]
	v_mfma_f32_16x16x32_bf16 v[26:29], v[78:81], v[200:203], v[26:29]
	v_mfma_f32_16x16x32_bf16 v[14:17], v[70:73], v[208:211], v[14:17]
	v_mfma_f32_16x16x32_bf16 v[10:13], v[78:81], v[208:211], v[10:13]
	v_mfma_f32_16x16x32_bf16 v[54:57], v[156:159], v[180:183], v[54:57]
	v_mfma_f32_16x16x32_bf16 v[50:53], v[172:175], v[180:183], v[50:53]
	v_mfma_f32_16x16x32_bf16 v[38:41], v[156:159], v[188:191], v[38:41]
	v_mfma_f32_16x16x32_bf16 v[34:37], v[172:175], v[188:191], v[34:37]
	v_mfma_f32_16x16x32_bf16 v[22:25], v[156:159], v[196:199], v[22:25]
	v_mfma_f32_16x16x32_bf16 v[18:21], v[172:175], v[196:199], v[18:21]
	v_mfma_f32_16x16x32_bf16 v[6:9], v[156:159], v[204:207], v[6:9]
	v_mfma_f32_16x16x32_bf16 v[2:5], v[172:175], v[204:207], v[2:5]
	v_mfma_f32_16x16x32_bf16 v[54:57], v[160:163], v[184:187], v[54:57]
	v_mfma_f32_16x16x32_bf16 v[50:53], v[176:179], v[184:187], v[50:53]
	v_mfma_f32_16x16x32_bf16 v[38:41], v[160:163], v[192:195], v[38:41]
	v_mfma_f32_16x16x32_bf16 v[34:37], v[176:179], v[192:195], v[34:37]
	v_mfma_f32_16x16x32_bf16 v[22:25], v[160:163], v[200:203], v[22:25]
	v_mfma_f32_16x16x32_bf16 v[18:21], v[176:179], v[200:203], v[18:21]
	v_mfma_f32_16x16x32_bf16 v[6:9], v[160:163], v[208:211], v[6:9]
	v_mfma_f32_16x16x32_bf16 v[2:5], v[176:179], v[208:211], v[2:5]
	s_barrier
	s_setprio 0
	s_add_i32 s2, 0, 0x18000
	s_add_i32 s68, 0, 0x1c000
	v_add_u32_e32 v78, s2, v168
	v_add_u32_e32 v171, s68, v168
	ds_read_b128 v[66:69], v78
	ds_read_b128 v[70:73], v78 offset:1024
	ds_read_b128 v[74:77], v78 offset:2048
	ds_read_b128 v[78:81], v78 offset:3072
	ds_read_b128 v[156:159], v171
	ds_read_b128 v[160:163], v171 offset:1024
	ds_read_b128 v[172:175], v171 offset:2048
	ds_read_b128 v[176:179], v171 offset:3072
	s_add_u32 s14, s14, 0x40000
	s_addc_u32 s15, s15, 0
	s_mov_b32 m0, s51
	v_lshl_add_u64 v[218:219], s[14:15], 0, v[150:151]
	ds_read_b128 v[180:183], v170 offset:32768
	ds_read_b128 v[184:187], v170 offset:33792
	ds_read_b128 v[188:191], v170 offset:34816
	ds_read_b128 v[192:195], v170 offset:35840
	ds_read_b128 v[196:199], v170 offset:36864
	ds_read_b128 v[200:203], v170 offset:37888
	ds_read_b128 v[204:207], v170 offset:38912
	ds_read_b128 v[208:211], v170 offset:39936
	global_load_lds_dwordx4 v[218:219], off
	v_lshl_add_u64 v[218:219], s[14:15], 0, v[148:149]
	s_mov_b32 m0, s52
	s_nop 0
	global_load_lds_dwordx4 v[218:219], off
	s_waitcnt vmcnt(8)
	s_waitcnt lgkmcnt(0)
	s_setprio 1
	s_barrier
	v_mfma_f32_16x16x32_bf16 v[142:145], v[66:69], v[180:183], v[142:145]
	v_mfma_f32_16x16x32_bf16 v[138:141], v[74:77], v[180:183], v[138:141]
	v_mfma_f32_16x16x32_bf16 v[126:129], v[66:69], v[188:191], v[126:129]
	v_mfma_f32_16x16x32_bf16 v[122:125], v[74:77], v[188:191], v[122:125]
	v_mfma_f32_16x16x32_bf16 v[110:113], v[66:69], v[196:199], v[110:113]
	v_mfma_f32_16x16x32_bf16 v[106:109], v[74:77], v[196:199], v[106:109]
	v_mfma_f32_16x16x32_bf16 v[94:97], v[66:69], v[204:207], v[94:97]
	v_mfma_f32_16x16x32_bf16 v[90:93], v[74:77], v[204:207], v[90:93]
	v_mfma_f32_16x16x32_bf16 v[142:145], v[70:73], v[184:187], v[142:145]
	v_mfma_f32_16x16x32_bf16 v[138:141], v[78:81], v[184:187], v[138:141]
	v_mfma_f32_16x16x32_bf16 v[126:129], v[70:73], v[192:195], v[126:129]
	v_mfma_f32_16x16x32_bf16 v[122:125], v[78:81], v[192:195], v[122:125]
	v_mfma_f32_16x16x32_bf16 v[110:113], v[70:73], v[200:203], v[110:113]
	v_mfma_f32_16x16x32_bf16 v[106:109], v[78:81], v[200:203], v[106:109]
	v_mfma_f32_16x16x32_bf16 v[94:97], v[70:73], v[208:211], v[94:97]
	v_mfma_f32_16x16x32_bf16 v[90:93], v[78:81], v[208:211], v[90:93]
	v_mfma_f32_16x16x32_bf16 v[134:137], v[156:159], v[180:183], v[134:137]
	v_mfma_f32_16x16x32_bf16 v[130:133], v[172:175], v[180:183], v[130:133]
	v_mfma_f32_16x16x32_bf16 v[118:121], v[156:159], v[188:191], v[118:121]
	v_mfma_f32_16x16x32_bf16 v[114:117], v[172:175], v[188:191], v[114:117]
	v_mfma_f32_16x16x32_bf16 v[102:105], v[156:159], v[196:199], v[102:105]
	v_mfma_f32_16x16x32_bf16 v[98:101], v[172:175], v[196:199], v[98:101]
	v_mfma_f32_16x16x32_bf16 v[86:89], v[156:159], v[204:207], v[86:89]
	v_mfma_f32_16x16x32_bf16 v[82:85], v[172:175], v[204:207], v[82:85]
	v_mfma_f32_16x16x32_bf16 v[134:137], v[160:163], v[184:187], v[134:137]
	v_mfma_f32_16x16x32_bf16 v[130:133], v[176:179], v[184:187], v[130:133]
	v_mfma_f32_16x16x32_bf16 v[118:121], v[160:163], v[192:195], v[118:121]
	v_mfma_f32_16x16x32_bf16 v[114:117], v[176:179], v[192:195], v[114:117]
	v_mfma_f32_16x16x32_bf16 v[102:105], v[160:163], v[200:203], v[102:105]
	v_mfma_f32_16x16x32_bf16 v[98:101], v[176:179], v[200:203], v[98:101]
	v_mfma_f32_16x16x32_bf16 v[86:89], v[160:163], v[208:211], v[86:89]
	v_mfma_f32_16x16x32_bf16 v[82:85], v[176:179], v[208:211], v[82:85]
	s_barrier
; #define PG8_STAGE(bufoff, gbase, voff) do { _Pragma("unroll") for (int _i = 0; _i < 2; ++_i) \
;         __builtin_amdgcn_global_load_lds((const unsigned*)((const char*)(gbase) + (voff)[_i]), (PG8_LAS unsigned*)(lds + (bufoff) + ldsw + _i * 8192), 16, 0, 0); } while (0)
; #define PG8_LDA(dst, b, h) do { _Pragma("unroll") for (int m = 0; m < 4; ++m) _Pragma("unroll") for (int k = 0; k < 2; ++k) dst[m][k] = *(const PG8_LAS bf16x8*)(lds + PG8_SA(b, h) + aoff + m * 2048 + k * 1024); } while (0)
; #define PG8_MMA(ai, bj, At, Bt) do { __builtin_amdgcn_s_setprio(1); _Pragma("unroll") for (int m = 0; m < 4; ++m) _Pragma("unroll") for (int n = 0; n < 2; ++n) _Pragma("unroll") for (int k = 0; k < 2; ++k) \
;         acc[ai][bj][m][n] = __builtin_amdgcn_mfma_f32_16x16x32_bf16(Bt[n][k], At[m][k], acc[ai][bj][m][n], 0, 0, 0); __builtin_amdgcn_s_setprio(0); } while (0)
; #define PG8_WAIT_V(n) asm volatile("s_waitcnt vmcnt(" #n ")" ::: "memory")
; #define PG8_WAIT_L(n) asm volatile("s_waitcnt lgkmcnt(" #n ")" ::: "memory")
; #define PG8_BAR __builtin_amdgcn_s_barrier()
; #define PG8_SCHED __builtin_amdgcn_sched_barrier(0)
; template <class Epi, class Sched, bool ALIGN_EPI = false, bool SP2 = false, bool GATHER = false>
; __device__ __forceinline__ void gemm_phase(PG8_LAS unsigned char* lds, const Gemm g, const Sched& S, const Epi& E, const int2* gslot = nullptr, PG8_LAS unsigned char* gtab = nullptr) {
;     ...
;             PG8_LDA(At, 1, 1); PG8_STAGE(PG8_SB(1, 0), b3, voffB); PG8_STAGE(PG8_SB(1, 1), b3 + hstep, voffB); PG8_STAGE(PG8_SA(1, 0), a3, PG8_VA(vS, 0));
;             PG8_WAIT_V(8); PG8_WAIT_L(0); PG8_BAR; PG8_MMA(1, 0, At, B0); PG8_MMA(1, 1, At, B1); PG8_BAR; PG8_SCHED;
;     ...
;         if constexpr (ALIGN_EPI) { if (wr == 0) PG8_BAR; }
	s_setprio 0
	s_add_i32 s2, s2, s45
	v_lshl_add_u64 v[164:165], v[164:165], 0, s[54:55]
	s_mov_b32 m0, s2
	ds_read_b128 v[180:183], v170 offset:49152
	ds_read_b128 v[184:187], v170 offset:50176
	ds_read_b128 v[188:191], v170 offset:51200
	ds_read_b128 v[192:195], v170 offset:52224
	ds_read_b128 v[196:199], v170 offset:53248
	ds_read_b128 v[200:203], v170 offset:54272
	ds_read_b128 v[204:207], v170 offset:55296
	ds_read_b128 v[208:211], v170 offset:56320
	global_load_lds_dwordx4 v[164:165], off
	s_add_i32 m0, s2, 0x2000
	s_add_u32 s10, s10, 0x40080
	v_lshl_add_u64 v[164:165], v[212:213], 0, s[54:55]
	s_addc_u32 s11, s11, 0
	s_add_i32 s2, s68, s45
	global_load_lds_dwordx4 v[164:165], off
	v_lshl_add_u64 v[164:165], s[10:11], 0, v[0:1]
	s_mov_b32 m0, s2
	s_nop 0
	global_load_lds_dwordx4 v[164:165], off
	v_lshl_add_u64 v[164:165], s[10:11], 0, v[146:147]
	s_add_i32 m0, s2, 0x2000
	s_nop 0
	global_load_lds_dwordx4 v[164:165], off
	v_lshl_add_u64 v[164:165], v[214:215], 0, s[54:55]
	s_mov_b32 m0, s58
	s_nop 0
	global_load_lds_dwordx4 v[164:165], off
	v_lshl_add_u64 v[164:165], v[216:217], 0, s[54:55]
	s_mov_b32 m0, s59
	s_nop 0
	global_load_lds_dwordx4 v[164:165], off
	s_waitcnt vmcnt(8)
	s_waitcnt lgkmcnt(0)
	s_setprio 1
	s_barrier
	v_mfma_f32_16x16x32_bf16 v[62:65], v[66:69], v[180:183], v[62:65]
	v_mfma_f32_16x16x32_bf16 v[58:61], v[74:77], v[180:183], v[58:61]
	v_mfma_f32_16x16x32_bf16 v[46:49], v[66:69], v[188:191], v[46:49]
	v_mfma_f32_16x16x32_bf16 v[42:45], v[74:77], v[188:191], v[42:45]
	v_mfma_f32_16x16x32_bf16 v[30:33], v[66:69], v[196:199], v[30:33]
	v_mfma_f32_16x16x32_bf16 v[26:29], v[74:77], v[196:199], v[26:29]
	v_mfma_f32_16x16x32_bf16 v[14:17], v[66:69], v[204:207], v[14:17]
	v_mfma_f32_16x16x32_bf16 v[10:13], v[74:77], v[204:207], v[10:13]
	v_mfma_f32_16x16x32_bf16 v[62:65], v[70:73], v[184:187], v[62:65]
	v_mfma_f32_16x16x32_bf16 v[58:61], v[78:81], v[184:187], v[58:61]
	v_mfma_f32_16x16x32_bf16 v[46:49], v[70:73], v[192:195], v[46:49]
	v_mfma_f32_16x16x32_bf16 v[42:45], v[78:81], v[192:195], v[42:45]
	v_mfma_f32_16x16x32_bf16 v[30:33], v[70:73], v[200:203], v[30:33]
	v_mfma_f32_16x16x32_bf16 v[26:29], v[78:81], v[200:203], v[26:29]
	v_mfma_f32_16x16x32_bf16 v[14:17], v[70:73], v[208:211], v[14:17]
	v_mfma_f32_16x16x32_bf16 v[10:13], v[78:81], v[208:211], v[10:13]
	v_mfma_f32_16x16x32_bf16 v[54:57], v[156:159], v[180:183], v[54:57]
	v_mfma_f32_16x16x32_bf16 v[50:53], v[172:175], v[180:183], v[50:53]
	v_mfma_f32_16x16x32_bf16 v[38:41], v[156:159], v[188:191], v[38:41]
	v_mfma_f32_16x16x32_bf16 v[34:37], v[172:175], v[188:191], v[34:37]
	v_mfma_f32_16x16x32_bf16 v[22:25], v[156:159], v[196:199], v[22:25]
	v_mfma_f32_16x16x32_bf16 v[18:21], v[172:175], v[196:199], v[18:21]
	v_mfma_f32_16x16x32_bf16 v[6:9], v[156:159], v[204:207], v[6:9]
	v_mfma_f32_16x16x32_bf16 v[2:5], v[172:175], v[204:207], v[2:5]
	v_mfma_f32_16x16x32_bf16 v[54:57], v[160:163], v[184:187], v[54:57]
	v_mfma_f32_16x16x32_bf16 v[50:53], v[176:179], v[184:187], v[50:53]
	v_mfma_f32_16x16x32_bf16 v[38:41], v[160:163], v[192:195], v[38:41]
	v_mfma_f32_16x16x32_bf16 v[34:37], v[176:179], v[192:195], v[34:37]
	v_mfma_f32_16x16x32_bf16 v[22:25], v[160:163], v[200:203], v[22:25]
	v_mfma_f32_16x16x32_bf16 v[18:21], v[176:179], v[200:203], v[18:21]
	v_mfma_f32_16x16x32_bf16 v[6:9], v[160:163], v[208:211], v[6:9]
	v_mfma_f32_16x16x32_bf16 v[2:5], v[176:179], v[208:211], v[2:5]
	s_barrier
	s_setprio 0
	s_add_i32 s67, s67, 2
	s_add_u32 s12, s12, 0x100
	s_addc_u32 s13, s13, 0
	s_add_u32 s27, s27, 0x100
	s_addc_u32 s29, s29, 0
	s_cmp_gt_u32 s67, 13
	s_cbranch_scc0 .LBB0_1174
	s_and_b64 vcc, exec, s[24:25]
	s_cbranch_vccz .LBB0_1177
	s_barrier
